# stack23 plus the first four V transposed reads of every step (operands of the first two P.V MFMAs) issued right after the last QK MFMA; waits unchanged
# speedup vs baseline: 1.0042x; 1.0042x over previous
; DI void finishSM(f32x16& p0, f32x16& p1, float alpha, float& l_reg, bf16x8& pa0, bf16x8& pa1, bf16x8& pa2, bf16x8& pa3) {
; #pragma unroll
;     for (int r = 0; r < 16; ++r) p1[r] = __builtin_amdgcn_exp2f(p1[r]);
;     float ps = 0;
; #pragma unroll
;     for (int r = 0; r < 16; ++r) ps += p0[r];
; #pragma unroll
;     for (int r = 0; r < 16; ++r) ps += p1[r];
;     { auto rr = __builtin_amdgcn_permlane32_swap(__float_as_uint(ps), __float_as_uint(ps), false, false); ps = __uint_as_float(rr[0]) + __uint_as_float(rr[1]); }
;     l_reg = l_reg * alpha + ps;
;     ...
;     AT_PK4(p0, 0, pa0); AT_PK4(p0, 8, pa1); AT_PK4(p1, 0, pa2); AT_PK4(p1, 8, pa3);
;     ...
; }
; DI void qkt(f32x16& p0, f32x16& p1, const char* Ks, const bf16x8* qr, const f32x16& negm, int r32, int hi) {
; #pragma unroll
;     for (int d0 = 0; d0 < 4; ++d0) { const int cb = (d0 * 16 + hi * 8) * 2;
;         const bf16x8 b0 = *reinterpret_cast<const bf16x8*>(Ks + AT_KSWZ(r32, cb));
;         const bf16x8 b1 = *reinterpret_cast<const bf16x8*>(Ks + AT_KSWZ(32 + r32, cb));
;         p0 = __builtin_amdgcn_mfma_f32_32x32x16_bf16(b0, qr[d0], d0 == 0 ? negm : p0, 0, 0, 0);
;         p1 = __builtin_amdgcn_mfma_f32_32x32x16_bf16(b1, qr[d0], d0 == 0 ? negm : p1, 0, 0, 0); }
; }
; DI void pv_all_sm(f32x16* o, int vb, bf16x8 pa0, bf16x8 pa1, bf16x8 pa2, bf16x8 pa3, f32x16& p0, f32x16& p1, float& m_ref, f32x16& negm, float& alpha) {
;     pv_one<0>(o[0], vb, pa0, pa1, pa2, pa3);
;     float pmax = p0[0];
; #pragma unroll
;     for (int r = 1; r < 16; ++r) pmax = fmaxf(pmax, p0[r]);
;     pv_one<1>(o[1], vb, pa0, pa1, pa2, pa3);
; #pragma unroll
;     for (int r = 0; r < 16; ++r) pmax = fmaxf(pmax, p1[r]);
;     { auto rr = __builtin_amdgcn_permlane32_swap(__float_as_uint(pmax), __float_as_uint(pmax), false, false); pmax = fmaxf(__uint_as_float(rr[0]), __uint_as_float(rr[1])); }
;     pv_one<2>(o[2], vb, pa0, pa1, pa2, pa3);
;     alpha = 1.f;
;     if (__builtin_expect(!__all(pmax <= THRL), 0)) {
.LBB4_702:
	s_lshl_b32 s26, s66, 13
	s_add_i32 s26, s26, 0
	v_add_u32_e32 v72, s26, v205
	v_add_u32_e32 v112, s26, v206
	v_add_u32_e32 v180, s26, v207
	s_waitcnt lgkmcnt(1)
	v_mfma_f32_32x32x16_bf16 v[128:143], v[64:67], v[156:159], v[80:95]
	ds_read_b128 v[64:67], v72 offset:49152
	ds_read_b128 v[72:75], v72 offset:53248
	ds_read_b128 v[76:79], v112 offset:49152
	ds_read_b128 v[220:223], v112 offset:53248
	s_add_u32 s74, s46, s28
	s_addc_u32 s75, s47, s29
	s_add_u32 s78, s74, 0x23808000
	s_addc_u32 s79, s75, 0
	s_add_u32 s80, s74, 0x2380a000
	s_add_u32 s76, s46, s30
	s_addc_u32 s77, s47, s31
	s_add_u32 s82, s76, 0x21804000
	s_addc_u32 s83, s77, 0
	s_lshl_b32 s92, s64, 14
	s_add_i32 s92, s92, s94
	s_mov_b32 m0, s92
	s_lshl_b32 s96, s64, 13
	global_load_lds_dwordx4 v249, s[78:79]
	s_addk_i32 s92, 0x400
	s_mov_b32 m0, s92
	s_add_i32 s96, s96, s95
	global_load_lds_dwordx4 v250, s[78:79]
	s_nop 0
	s_mov_b32 m0, s96
	s_nop 0
	global_load_lds_dwordx4 v251, s[82:83]
	v_exp_f32_e32 v186, v97
	v_exp_f32_e32 v213, v98
	v_exp_f32_e32 v214, v99
	v_exp_f32_e32 v219, v100
	v_exp_f32_e32 v228, v101
	s_waitcnt lgkmcnt(4)
	v_mfma_f32_32x32x16_bf16 v[112:127], v[68:71], v[156:159], v[80:95]
	ds_read_b128 v[68:71], v180 offset:49152
	ds_read_b128 v[224:227], v180 offset:53248
	v_exp_f32_e32 v180, v96
	v_cvt_pk_bf16_f32 v96, v216, v218
	v_cvt_pk_bf16_f32 v97, v179, v217
	v_cvt_pk_bf16_f32 v98, v177, v215
	v_cvt_pk_bf16_f32 v99, v176, v178
	s_waitcnt lgkmcnt(4)
	v_mfma_f32_32x32x16_bf16 v[112:127], v[72:75], v[152:155], v[112:127]
	v_add_f32_e32 v75, 0, v216
	v_add_f32_e32 v75, v218, v75
	v_add_f32_e32 v75, v179, v75
	v_add_f32_e32 v75, v217, v75
	v_add_f32_e32 v75, v177, v75
	v_add_f32_e32 v75, v215, v75
	v_add_f32_e32 v75, v176, v75
	v_mfma_f32_32x32x16_bf16 v[128:143], v[64:67], v[152:155], v[128:143]
	v_add_f32_e32 v75, v178, v75
	v_add_f32_e32 v75, v173, v75
	v_add_f32_e32 v75, v175, v75
	v_add_f32_e32 v75, v171, v75
	v_add_f32_e32 v75, v174, v75
	v_add_f32_e32 v75, v169, v75
	v_add_f32_e32 v75, v172, v75
	s_waitcnt lgkmcnt(3)
	v_mfma_f32_32x32x16_bf16 v[128:143], v[76:79], v[148:151], v[128:143]
	v_add_f32_e32 v75, v168, v75
	v_add_f32_e32 v75, v170, v75
	v_add_f32_e32 v75, v180, v75
	v_add_f32_e32 v75, v186, v75
	v_exp_f32_e32 v64, v102
	v_exp_f32_e32 v65, v103
	v_exp_f32_e32 v66, v104
	s_waitcnt lgkmcnt(2)
	v_mfma_f32_32x32x16_bf16 v[112:127], v[220:223], v[148:151], v[112:127]
	v_exp_f32_e32 v67, v105
	v_exp_f32_e32 v105, v106
	v_exp_f32_e32 v106, v107
	v_exp_f32_e32 v107, v108
	v_exp_f32_e32 v72, v109
	v_exp_f32_e32 v73, v110
	v_exp_f32_e32 v74, v111
	s_waitcnt lgkmcnt(1)
	v_mfma_f32_32x32x16_bf16 v[128:143], v[68:71], v[144:147], v[128:143]
	v_add_f32_e32 v68, v213, v75
	v_add_f32_e32 v68, v214, v68
	v_add_f32_e32 v68, v219, v68
	v_add_f32_e32 v68, v228, v68
	v_add_f32_e32 v68, v64, v68
	v_add_f32_e32 v68, v65, v68
	v_add_f32_e32 v68, v66, v68
	v_add_f32_e32 v68, v67, v68
	s_waitcnt lgkmcnt(0)
	v_mfma_f32_32x32x16_bf16 v[112:127], v[224:227], v[144:147], v[112:127]
	v_cvt_pk_bf16_f32 v100, v180, v186
	v_cvt_pk_bf16_f32 v103, v64, v65
	v_cvt_pk_bf16_f32 v104, v66, v67
	s_lshl_b32 s67, s65, 14
	v_add_u32_e32 v186, s67, v253
	ds_read_b64_tr_b16 v[64:65], v186 offset:0
	ds_read_b64_tr_b16 v[66:67], v186 offset:0x100
	v_add_f32_e32 v68, v105, v68
	v_add_f32_e32 v68, v106, v68
	v_add_f32_e32 v68, v107, v68
	v_add_f32_e32 v68, v72, v68
	v_add_f32_e32 v68, v73, v68
	v_add_f32_e32 v183, v74, v68
	ds_read_b64_tr_b16 v[68:69], v186 offset:0x1000
	ds_read_b64_tr_b16 v[70:71], v186 offset:0x1100
	v_cvt_pk_bf16_f32 v108, v173, v175
	v_cvt_pk_bf16_f32 v109, v171, v174
	v_cvt_pk_bf16_f32 v110, v169, v172
	v_cvt_pk_bf16_f32 v111, v168, v170
	v_cvt_pk_bf16_f32 v101, v213, v214
	v_cvt_pk_bf16_f32 v102, v219, v228
	v_cvt_pk_bf16_f32 v105, v105, v106
	v_cvt_pk_bf16_f32 v106, v107, v72
	v_cvt_pk_bf16_f32 v107, v73, v74
	s_addc_u32 s81, s75, 0
	s_andn2_b64 vcc, exec, s[2:3]
	s_cbranch_vccnz .LBB4_704
	s_mov_b64 s[2:3], s[8:9]
	global_store_dwordx2 v189, v[184:185], s[2:3] nt
.LBB4_704:
	ds_read_b64_tr_b16 v[72:73], v186 offset:0x2000
	ds_read_b64_tr_b16 v[74:75], v186 offset:0x2100
	ds_read_b64_tr_b16 v[76:77], v186 offset:0x3000
	ds_read_b64_tr_b16 v[78:79], v186 offset:0x3100
	s_waitcnt lgkmcnt(0)
	v_mfma_f32_32x32x16_bf16 v[32:47], v[64:67], v[96:99], v[32:47]
	v_max_f32_e32 v64, v128, v129
	v_max3_f32 v64, v64, v130, v131
	v_max3_f32 v64, v64, v132, v133
	v_max3_f32 v64, v64, v134, v135
	v_max3_f32 v64, v64, v136, v137
	v_mfma_f32_32x32x16_bf16 v[32:47], v[68:71], v[108:111], v[32:47]
	v_max3_f32 v64, v64, v138, v139
	v_max3_f32 v66, v64, v140, v141
	ds_read_b64_tr_b16 v[64:65], v186 offset:0x200
	v_max3_f32 v180, v66, v142, v143
	ds_read_b64_tr_b16 v[66:67], v186 offset:0x300
	ds_read_b64_tr_b16 v[68:69], v186 offset:0x1200
	ds_read_b64_tr_b16 v[70:71], v186 offset:0x1300
	v_mfma_f32_32x32x16_bf16 v[32:47], v[72:75], v[100:103], v[32:47]
	ds_read_b64_tr_b16 v[72:73], v186 offset:0x2200
	ds_read_b64_tr_b16 v[74:75], v186 offset:0x2300
	ds_read_b64_tr_b16 v[214:215], v186 offset:0x3200
	ds_read_b64_tr_b16 v[216:217], v186 offset:0x3300
	v_mfma_f32_32x32x16_bf16 v[32:47], v[76:79], v[104:107], v[32:47]
	s_waitcnt lgkmcnt(0)
	v_mfma_f32_32x32x16_bf16 v[48:63], v[64:67], v[96:99], v[48:63]
	v_max3_f32 v76, v180, v112, v113
	v_max3_f32 v64, v76, v114, v115
	ds_read_b64_tr_b16 v[66:67], v186 offset:0x400
	v_max3_f32 v64, v64, v116, v117
	v_max3_f32 v64, v64, v118, v119
	v_max3_f32 v64, v64, v120, v121
	v_max3_f32 v64, v64, v122, v123
	v_mfma_f32_32x32x16_bf16 v[48:63], v[68:71], v[108:111], v[48:63]
	ds_read_b64_tr_b16 v[68:69], v186 offset:0x500
	ds_read_b64_tr_b16 v[70:71], v186 offset:0x1400
	v_max3_f32 v64, v64, v124, v125
	v_max3_f32 v64, v64, v126, v127
	v_mov_b32_e32 v65, v64
	s_nop 1
	v_permlane32_swap_b32_e32 v64, v65
	v_mfma_f32_32x32x16_bf16 v[48:63], v[72:75], v[100:103], v[48:63]
	ds_read_b64_tr_b16 v[72:73], v186 offset:0x1500
	ds_read_b64_tr_b16 v[74:75], v186 offset:0x2400
	ds_read_b64_tr_b16 v[76:77], v186 offset:0x2500
	ds_read_b64_tr_b16 v[218:219], v186 offset:0x3400
	ds_read_b64_tr_b16 v[220:221], v186 offset:0x3500
	v_mfma_f32_32x32x16_bf16 v[48:63], v[214:217], v[104:107], v[48:63]
	s_waitcnt lgkmcnt(0)
	v_max_f32_e32 v64, v64, v65
	v_mfma_f32_32x32x16_bf16 v[16:31], v[66:69], v[96:99], v[16:31]
	v_cmp_ge_f32_e32 vcc, s25, v64
	s_cmp_eq_u64 vcc, exec
	v_mfma_f32_32x32x16_bf16 v[16:31], v[70:73], v[108:111], v[16:31]
	v_mfma_f32_32x32x16_bf16 v[16:31], v[74:77], v[100:103], v[16:31]
	v_mfma_f32_32x32x16_bf16 v[16:31], v[218:221], v[104:107], v[16:31]
	s_cbranch_scc0 .LBB4_737
	v_mov_b32_e32 v180, 1.0

; template <int OFF> DI s16x4 tr_read(int vb) { s16x4 r; asm volatile("ds_read_b64_tr_b16 %0, %1 offset:%2" : "=&v"(r) : "v"(vb), "i"(OFF) : "memory"); return r; }
; DI void finishSM(f32x16& p0, f32x16& p1, float alpha, float& l_reg, bf16x8& pa0, bf16x8& pa1, bf16x8& pa2, bf16x8& pa3) {
; #pragma unroll
;     for (int r = 0; r < 16; ++r) p1[r] = __builtin_amdgcn_exp2f(p1[r]);
;     float ps = 0;
; #pragma unroll
;     for (int r = 0; r < 16; ++r) ps += p0[r];
; #pragma unroll
;     for (int r = 0; r < 16; ++r) ps += p1[r];
;     { auto rr = __builtin_amdgcn_permlane32_swap(__float_as_uint(ps), __float_as_uint(ps), false, false); ps = __uint_as_float(rr[0]) + __uint_as_float(rr[1]); }
;     l_reg = l_reg * alpha + ps;
;     ...
;     AT_PK4(p0, 0, pa0); AT_PK4(p0, 8, pa1); AT_PK4(p1, 0, pa2); AT_PK4(p1, 8, pa3);
;     ...
; }
; DI void qkt(f32x16& p0, f32x16& p1, const char* Ks, const bf16x8* qr, const f32x16& negm, int r32, int hi) {
; #pragma unroll
;     for (int d0 = 0; d0 < 4; ++d0) { const int cb = (d0 * 16 + hi * 8) * 2;
;         const bf16x8 b0 = *reinterpret_cast<const bf16x8*>(Ks + AT_KSWZ(r32, cb));
;         const bf16x8 b1 = *reinterpret_cast<const bf16x8*>(Ks + AT_KSWZ(32 + r32, cb));
;         p0 = __builtin_amdgcn_mfma_f32_32x32x16_bf16(b0, qr[d0], d0 == 0 ? negm : p0, 0, 0, 0);
;         p1 = __builtin_amdgcn_mfma_f32_32x32x16_bf16(b1, qr[d0], d0 == 0 ? negm : p1, 0, 0, 0); }
; }
; template <int D0> DI void pv_one(f32x16& od, int vb, bf16x8 pa0, bf16x8 pa1, bf16x8 pa2, bf16x8 pa3) {
;     const s16x4 l0 = tr_read<v_rd_off(D0, 0, 0)>(vb), h0 = tr_read<v_rd_off(D0, 0, 1)>(vb), l1 = tr_read<v_rd_off(D0, 1, 0)>(vb), h1 = tr_read<v_rd_off(D0, 1, 1)>(vb);
;     const s16x4 l2 = tr_read<v_rd_off(D0, 2, 0)>(vb), h2 = tr_read<v_rd_off(D0, 2, 1)>(vb), l3 = tr_read<v_rd_off(D0, 3, 0)>(vb), h3 = tr_read<v_rd_off(D0, 3, 1)>(vb);
.LBB4_723:
	v_exp_f32_e32 v186, v128
	v_exp_f32_e32 v230, v129
	v_exp_f32_e32 v231, v130
	v_exp_f32_e32 v232, v131
	v_exp_f32_e32 v233, v132
	v_exp_f32_e32 v234, v133
	v_exp_f32_e32 v235, v134
	v_exp_f32_e32 v236, v135
	v_exp_f32_e32 v237, v136
	v_exp_f32_e32 v238, v137
	v_exp_f32_e32 v239, v138
	v_exp_f32_e32 v240, v139
	v_exp_f32_e32 v241, v140
	v_exp_f32_e32 v242, v141
	v_exp_f32_e32 v243, v142
	v_exp_f32_e32 v244, v143
	v_add_u32_e32 v101, s78, v205
	v_add_u32_e32 v102, s78, v206
	v_add_u32_e32 v103, s78, v207
	ds_read_b128 v[172:175], v101 offset:49152
	ds_read_b128 v[176:179], v101 offset:53248
	ds_read_b128 v[214:217], v102 offset:49152
	ds_read_b128 v[218:221], v102 offset:53248
	ds_read_b128 v[222:225], v103 offset:49152
	ds_read_b128 v[226:229], v103 offset:53248
	v_exp_f32_e32 v112, v112
	v_exp_f32_e32 v113, v113
	v_exp_f32_e32 v114, v114
	s_waitcnt lgkmcnt(7)
	v_mfma_f32_32x32x16_bf16 v[128:143], v[96:99], v[156:159], v[80:95]
	s_add_u32 s78, s74, 0x2380c000
	s_addc_u32 s79, s75, 0
	s_add_u32 s74, s74, 0x2380e000
	s_addc_u32 s75, s75, 0
	s_add_u32 s76, s76, 0x21806000
	s_addc_u32 s77, s77, 0
	s_lshl_b32 s92, s65, 14
	s_add_i32 s92, s92, s94
	s_mov_b32 m0, s92
	s_lshl_b32 s96, s65, 13
	global_load_lds_dwordx4 v249, s[78:79]
	s_addk_i32 s92, 0x400
	s_mov_b32 m0, s92
	s_add_i32 s96, s96, s95
	global_load_lds_dwordx4 v250, s[78:79]
	s_nop 0
	s_mov_b32 m0, s96
	s_nop 0
	global_load_lds_dwordx4 v251, s[76:77]
	s_nop 0
	v_exp_f32_e32 v115, v115
	v_exp_f32_e32 v116, v116
	v_exp_f32_e32 v117, v117
	v_exp_f32_e32 v118, v118
	v_exp_f32_e32 v119, v119
	s_waitcnt lgkmcnt(6)
	v_mfma_f32_32x32x16_bf16 v[96:111], v[168:171], v[156:159], v[80:95]
	v_exp_f32_e32 v168, v120
	v_add_f32_e32 v120, 0, v186
	v_add_f32_e32 v120, v230, v120
	v_add_f32_e32 v120, v231, v120
	v_add_f32_e32 v120, v232, v120
	v_add_f32_e32 v120, v233, v120
	v_add_f32_e32 v120, v234, v120
	v_add_f32_e32 v120, v235, v120
	v_add_f32_e32 v120, v236, v120
	v_add_f32_e32 v120, v237, v120
	v_add_f32_e32 v120, v238, v120
	s_waitcnt lgkmcnt(5)
	v_mfma_f32_32x32x16_bf16 v[128:143], v[172:175], v[152:155], v[128:143]
	v_add_f32_e32 v120, v239, v120
	v_add_f32_e32 v120, v240, v120
	v_add_f32_e32 v120, v241, v120
	v_add_f32_e32 v120, v242, v120
	v_add_f32_e32 v120, v243, v120
	v_add_f32_e32 v120, v244, v120
	v_add_f32_e32 v120, v112, v120
	s_waitcnt lgkmcnt(4)
	v_mfma_f32_32x32x16_bf16 v[96:111], v[176:179], v[152:155], v[96:111]
	v_add_f32_e32 v120, v113, v120
	v_add_f32_e32 v120, v114, v120
	v_add_f32_e32 v120, v115, v120
	v_add_f32_e32 v120, v116, v120
	v_exp_f32_e32 v169, v121
	v_add_f32_e32 v120, v117, v120
	v_exp_f32_e32 v170, v122
	s_waitcnt lgkmcnt(3)
	v_mfma_f32_32x32x16_bf16 v[128:143], v[214:217], v[148:151], v[128:143]
	v_add_f32_e32 v120, v118, v120
	v_exp_f32_e32 v171, v123
	v_add_f32_e32 v120, v119, v120
	v_exp_f32_e32 v172, v124
	v_add_f32_e32 v120, v168, v120
	v_exp_f32_e32 v173, v125
	v_add_f32_e32 v120, v169, v120
	s_waitcnt lgkmcnt(2)
	v_mfma_f32_32x32x16_bf16 v[96:111], v[218:221], v[148:151], v[96:111]
	v_exp_f32_e32 v174, v126
	v_add_f32_e32 v120, v170, v120
	v_exp_f32_e32 v175, v127
	v_add_f32_e32 v120, v171, v120
	v_add_f32_e32 v120, v172, v120
	v_add_f32_e32 v120, v173, v120
	v_add_f32_e32 v120, v174, v120
	s_waitcnt lgkmcnt(1)
	v_mfma_f32_32x32x16_bf16 v[128:143], v[222:225], v[144:147], v[128:143]
	v_add_f32_e32 v213, v175, v120
	v_cvt_pk_bf16_f32 v120, v186, v230
	v_cvt_pk_bf16_f32 v121, v231, v232
	v_cvt_pk_bf16_f32 v122, v233, v234
	v_cvt_pk_bf16_f32 v123, v235, v236
	v_cvt_pk_bf16_f32 v124, v237, v238
	s_waitcnt lgkmcnt(0)
	v_mfma_f32_32x32x16_bf16 v[96:111], v[226:229], v[144:147], v[96:111]
	v_lshl_add_u32 v215, s66, 14, v253
	ds_read_b64_tr_b16 v[216:217], v215 offset:0
	ds_read_b64_tr_b16 v[218:219], v215 offset:0x100
	ds_read_b64_tr_b16 v[220:221], v215 offset:0x1000
	ds_read_b64_tr_b16 v[222:223], v215 offset:0x1100
	v_cvt_pk_bf16_f32 v125, v239, v240
	v_cvt_pk_bf16_f32 v126, v241, v242
	v_cvt_pk_bf16_f32 v127, v243, v244
	v_cvt_pk_bf16_f32 v112, v112, v113
	v_cvt_pk_bf16_f32 v113, v114, v115
	v_cvt_pk_bf16_f32 v114, v116, v117
	v_cvt_pk_bf16_f32 v115, v118, v119
	v_cvt_pk_bf16_f32 v116, v168, v169
	v_cvt_pk_bf16_f32 v117, v170, v171
	v_cvt_pk_bf16_f32 v118, v172, v173
	v_cvt_pk_bf16_f32 v119, v174, v175
	s_and_b64 vcc, exec, s[2:3]
	s_cbranch_vccnz .LBB4_725
	s_mov_b64 s[2:3], s[8:9]
	global_store_dwordx2 v189, v[184:185], s[2:3] nt
; #define AT_SBAR() __builtin_amdgcn_sched_barrier(0)
; template <int OFF> DI s16x4 tr_read(int vb) { s16x4 r; asm volatile("ds_read_b64_tr_b16 %0, %1 offset:%2" : "=&v"(r) : "v"(vb), "i"(OFF) : "memory"); return r; }
; template <int D0> DI void pv_one(f32x16& od, int vb, bf16x8 pa0, bf16x8 pa1, bf16x8 pa2, bf16x8 pa3) {
;     const s16x4 l0 = tr_read<v_rd_off(D0, 0, 0)>(vb), h0 = tr_read<v_rd_off(D0, 0, 1)>(vb), l1 = tr_read<v_rd_off(D0, 1, 0)>(vb), h1 = tr_read<v_rd_off(D0, 1, 1)>(vb);
;     const s16x4 l2 = tr_read<v_rd_off(D0, 2, 0)>(vb), h2 = tr_read<v_rd_off(D0, 2, 1)>(vb), l3 = tr_read<v_rd_off(D0, 3, 0)>(vb), h3 = tr_read<v_rd_off(D0, 3, 1)>(vb);
;     asm volatile("s_waitcnt lgkmcnt(0)" ::: "memory"); AT_SBAR();
;     ...
;     od = __builtin_amdgcn_mfma_f32_32x32x16_bf16(AT_PK(l0, h0), pa0, od, 0, 0, 0);
;     od = __builtin_amdgcn_mfma_f32_32x32x16_bf16(AT_PK(l1, h1), pa1, od, 0, 0, 0);
;     od = __builtin_amdgcn_mfma_f32_32x32x16_bf16(AT_PK(l2, h2), pa2, od, 0, 0, 0);
;     od = __builtin_amdgcn_mfma_f32_32x32x16_bf16(AT_PK(l3, h3), pa3, od, 0, 0, 0);
;     ...
; }
; DI void pv_all_sm(f32x16* o, int vb, bf16x8 pa0, bf16x8 pa1, bf16x8 pa2, bf16x8 pa3, f32x16& p0, f32x16& p1, float& m_ref, f32x16& negm, float& alpha) {
;     pv_one<0>(o[0], vb, pa0, pa1, pa2, pa3);
;     float pmax = p0[0];
; #pragma unroll
;     for (int r = 1; r < 16; ++r) pmax = fmaxf(pmax, p0[r]);
;     pv_one<1>(o[1], vb, pa0, pa1, pa2, pa3);
; #pragma unroll
;     for (int r = 0; r < 16; ++r) pmax = fmaxf(pmax, p1[r]);
;     { auto rr = __builtin_amdgcn_permlane32_swap(__float_as_uint(pmax), __float_as_uint(pmax), false, false); pmax = fmaxf(__uint_as_float(rr[0]), __uint_as_float(rr[1])); }
;     pv_one<2>(o[2], vb, pa0, pa1, pa2, pa3);
;     alpha = 1.f;
;     if (__builtin_expect(!__all(pmax <= THRL), 0)) {
.LBB4_725:
	ds_read_b64_tr_b16 v[224:225], v215 offset:0x2000
	ds_read_b64_tr_b16 v[226:227], v215 offset:0x2100
	ds_read_b64_tr_b16 v[228:229], v215 offset:0x3000
	ds_read_b64_tr_b16 v[230:231], v215 offset:0x3100
	s_waitcnt lgkmcnt(0)
	v_mfma_f32_32x32x16_bf16 v[32:47], v[216:219], v[120:123], v[32:47]
	v_max_f32_e32 v186, v128, v129
	ds_read_b64_tr_b16 v[216:217], v215 offset:0x200
	ds_read_b64_tr_b16 v[218:219], v215 offset:0x300
	v_max3_f32 v186, v186, v130, v131
	v_max3_f32 v186, v186, v132, v133
	v_mfma_f32_32x32x16_bf16 v[32:47], v[220:223], v[124:127], v[32:47]
	ds_read_b64_tr_b16 v[220:221], v215 offset:0x1200
	ds_read_b64_tr_b16 v[222:223], v215 offset:0x1300
	v_max3_f32 v186, v186, v134, v135
	v_max3_f32 v186, v186, v136, v137
	v_max3_f32 v186, v186, v138, v139
	v_max3_f32 v186, v186, v140, v141
	v_max3_f32 v186, v186, v142, v143
	v_mfma_f32_32x32x16_bf16 v[32:47], v[224:227], v[112:115], v[32:47]
	ds_read_b64_tr_b16 v[224:225], v215 offset:0x2200
	ds_read_b64_tr_b16 v[226:227], v215 offset:0x2300
	ds_read_b64_tr_b16 v[232:233], v215 offset:0x3200
	ds_read_b64_tr_b16 v[234:235], v215 offset:0x3300
	v_mfma_f32_32x32x16_bf16 v[32:47], v[228:231], v[116:119], v[32:47]
	s_waitcnt lgkmcnt(0)
	v_mfma_f32_32x32x16_bf16 v[48:63], v[216:219], v[120:123], v[48:63]
	v_max3_f32 v186, v186, v96, v97
	v_max3_f32 v186, v186, v98, v99
	ds_read_b64_tr_b16 v[218:219], v215 offset:0x400
	v_max3_f32 v186, v186, v100, v101
	v_max3_f32 v186, v186, v102, v103
	v_max3_f32 v186, v186, v104, v105
	v_max3_f32 v186, v186, v106, v107
	v_mfma_f32_32x32x16_bf16 v[48:63], v[220:223], v[124:127], v[48:63]
	ds_read_b64_tr_b16 v[220:221], v215 offset:0x500
	ds_read_b64_tr_b16 v[222:223], v215 offset:0x1400
	v_max3_f32 v186, v186, v108, v109
	v_max3_f32 v186, v186, v110, v111
	v_mov_b32_e32 v216, v186
	s_nop 1
	v_permlane32_swap_b32_e32 v186, v216
	v_mfma_f32_32x32x16_bf16 v[48:63], v[224:227], v[112:115], v[48:63]
	ds_read_b64_tr_b16 v[224:225], v215 offset:0x1500
	ds_read_b64_tr_b16 v[226:227], v215 offset:0x2400
	ds_read_b64_tr_b16 v[228:229], v215 offset:0x2500
	ds_read_b64_tr_b16 v[236:237], v215 offset:0x3400
	ds_read_b64_tr_b16 v[238:239], v215 offset:0x3500
	v_mfma_f32_32x32x16_bf16 v[48:63], v[232:235], v[116:119], v[48:63]
	s_waitcnt lgkmcnt(0)
	v_max_f32_e32 v216, v186, v216
	v_mfma_f32_32x32x16_bf16 v[16:31], v[218:221], v[120:123], v[16:31]
	v_cmp_ge_f32_e32 vcc, s25, v216
	s_cmp_eq_u64 vcc, exec
	v_mov_b32_e32 v186, 1.0
	v_mfma_f32_32x32x16_bf16 v[16:31], v[222:225], v[124:127], v[16:31]
	v_mfma_f32_32x32x16_bf16 v[16:31], v[226:229], v[112:115], v[16:31]
	v_mfma_f32_32x32x16_bf16 v[16:31], v[236:239], v[116:119], v[16:31]
	s_cbranch_scc0 .LBB4_738

; DI void finishSM(f32x16& p0, f32x16& p1, float alpha, float& l_reg, bf16x8& pa0, bf16x8& pa1, bf16x8& pa2, bf16x8& pa3) {
; #pragma unroll
;     for (int r = 0; r < 16; ++r) p1[r] = __builtin_amdgcn_exp2f(p1[r]);
;     float ps = 0;
; #pragma unroll
;     for (int r = 0; r < 16; ++r) ps += p0[r];
; #pragma unroll
;     for (int r = 0; r < 16; ++r) ps += p1[r];
;     { auto rr = __builtin_amdgcn_permlane32_swap(__float_as_uint(ps), __float_as_uint(ps), false, false); ps = __uint_as_float(rr[0]) + __uint_as_float(rr[1]); }
;     l_reg = l_reg * alpha + ps;
;     ...
;     AT_PK4(p0, 0, pa0); AT_PK4(p0, 8, pa1); AT_PK4(p1, 0, pa2); AT_PK4(p1, 8, pa3);
;     ...
; }
; DI void qkt(f32x16& p0, f32x16& p1, const char* Ks, const bf16x8* qr, const f32x16& negm, int r32, int hi) {
; #pragma unroll
;     for (int d0 = 0; d0 < 4; ++d0) { const int cb = (d0 * 16 + hi * 8) * 2;
;         const bf16x8 b0 = *reinterpret_cast<const bf16x8*>(Ks + AT_KSWZ(r32, cb));
;         const bf16x8 b1 = *reinterpret_cast<const bf16x8*>(Ks + AT_KSWZ(32 + r32, cb));
;         p0 = __builtin_amdgcn_mfma_f32_32x32x16_bf16(b0, qr[d0], d0 == 0 ? negm : p0, 0, 0, 0);
;         p1 = __builtin_amdgcn_mfma_f32_32x32x16_bf16(b1, qr[d0], d0 == 0 ? negm : p1, 0, 0, 0); }
; }
; DI void pv_all_sm(f32x16* o, int vb, bf16x8 pa0, bf16x8 pa1, bf16x8 pa2, bf16x8 pa3, f32x16& p0, f32x16& p1, float& m_ref, f32x16& negm, float& alpha) {
;     pv_one<0>(o[0], vb, pa0, pa1, pa2, pa3);
;     float pmax = p0[0];
; #pragma unroll
;     for (int r = 1; r < 16; ++r) pmax = fmaxf(pmax, p0[r]);
;     pv_one<1>(o[1], vb, pa0, pa1, pa2, pa3);
; #pragma unroll
;     for (int r = 0; r < 16; ++r) pmax = fmaxf(pmax, p1[r]);
;     { auto rr = __builtin_amdgcn_permlane32_swap(__float_as_uint(pmax), __float_as_uint(pmax), false, false); pmax = fmaxf(__uint_as_float(rr[0]), __uint_as_float(rr[1])); }
;     pv_one<2>(o[2], vb, pa0, pa1, pa2, pa3);
;     alpha = 1.f;
;     if (__builtin_expect(!__all(pmax <= THRL), 0)) {
.LBB4_775:
	s_lshl_b32 s20, s30, 13
	s_add_i32 s20, s20, 0
	v_add_u32_e32 v72, s20, v208
	v_add_u32_e32 v112, s20, v209
	v_add_u32_e32 v180, s20, v210
	s_waitcnt lgkmcnt(1)
	v_mfma_f32_32x32x16_bf16 v[128:143], v[64:67], v[156:159], v[80:95]
	ds_read_b128 v[64:67], v72 offset:49152
	ds_read_b128 v[72:75], v72 offset:53248
	ds_read_b128 v[76:79], v112 offset:49152
	ds_read_b128 v[224:227], v112 offset:53248
	s_add_u32 s34, s46, s16
	s_addc_u32 s35, s47, s17
	s_add_u32 s24, s34, 0x23808000
	s_addc_u32 s25, s35, 0
	s_add_u32 s66, s34, 0x2380a000
	s_add_u32 s37, s46, s18
	s_addc_u32 s64, s47, s19
	s_add_u32 s74, s37, 0x21884000
	s_addc_u32 s75, s64, 0
	s_lshl_b32 s92, s15, 14
	s_add_i32 s92, s92, s94
	s_mov_b32 m0, s92
	s_lshl_b32 s96, s15, 13
	global_load_lds_dwordx4 v249, s[24:25]
	s_addk_i32 s92, 0x400
	s_mov_b32 m0, s92
	s_add_i32 s96, s96, s95
	global_load_lds_dwordx4 v250, s[24:25]
	s_nop 0
	s_mov_b32 m0, s96
	s_nop 0
	global_load_lds_dwordx4 v251, s[74:75]
	v_exp_f32_e32 v182, v97
	v_exp_f32_e32 v217, v98
	v_exp_f32_e32 v218, v99
	v_exp_f32_e32 v223, v100
	v_exp_f32_e32 v232, v101
	s_waitcnt lgkmcnt(4)
	v_mfma_f32_32x32x16_bf16 v[112:127], v[68:71], v[156:159], v[80:95]
	ds_read_b128 v[68:71], v180 offset:49152
	ds_read_b128 v[228:231], v180 offset:53248
	v_exp_f32_e32 v180, v96
	v_cvt_pk_bf16_f32 v96, v220, v222
	v_cvt_pk_bf16_f32 v97, v179, v221
	v_cvt_pk_bf16_f32 v98, v177, v219
	v_cvt_pk_bf16_f32 v99, v176, v178
	s_waitcnt lgkmcnt(4)
	v_mfma_f32_32x32x16_bf16 v[112:127], v[72:75], v[152:155], v[112:127]
	v_add_f32_e32 v75, 0, v220
	v_add_f32_e32 v75, v222, v75
	v_add_f32_e32 v75, v179, v75
	v_add_f32_e32 v75, v221, v75
	v_add_f32_e32 v75, v177, v75
	v_add_f32_e32 v75, v219, v75
	v_add_f32_e32 v75, v176, v75
	v_mfma_f32_32x32x16_bf16 v[128:143], v[64:67], v[152:155], v[128:143]
	v_add_f32_e32 v75, v178, v75
	v_add_f32_e32 v75, v173, v75
	v_add_f32_e32 v75, v175, v75
	v_add_f32_e32 v75, v171, v75
	v_add_f32_e32 v75, v174, v75
	v_add_f32_e32 v75, v169, v75
	v_add_f32_e32 v75, v172, v75
	s_waitcnt lgkmcnt(3)
	v_mfma_f32_32x32x16_bf16 v[128:143], v[76:79], v[148:151], v[128:143]
	v_add_f32_e32 v75, v168, v75
	v_add_f32_e32 v75, v170, v75
	v_add_f32_e32 v75, v180, v75
	v_add_f32_e32 v75, v182, v75
	v_exp_f32_e32 v64, v102
	v_exp_f32_e32 v65, v103
	v_exp_f32_e32 v66, v104
	s_waitcnt lgkmcnt(2)
	v_mfma_f32_32x32x16_bf16 v[112:127], v[224:227], v[148:151], v[112:127]
	v_exp_f32_e32 v67, v105
	v_exp_f32_e32 v105, v106
	v_exp_f32_e32 v106, v107
	v_exp_f32_e32 v107, v108
	v_exp_f32_e32 v72, v109
	v_exp_f32_e32 v73, v110
	v_exp_f32_e32 v74, v111
	s_waitcnt lgkmcnt(1)
	v_mfma_f32_32x32x16_bf16 v[128:143], v[68:71], v[144:147], v[128:143]
	v_add_f32_e32 v68, v217, v75
	v_add_f32_e32 v68, v218, v68
	v_add_f32_e32 v68, v223, v68
	v_add_f32_e32 v68, v232, v68
	v_add_f32_e32 v68, v64, v68
	v_add_f32_e32 v68, v65, v68
	v_add_f32_e32 v68, v66, v68
	v_add_f32_e32 v68, v67, v68
	s_waitcnt lgkmcnt(0)
	v_mfma_f32_32x32x16_bf16 v[112:127], v[228:231], v[144:147], v[112:127]
	v_cvt_pk_bf16_f32 v100, v180, v182
	v_cvt_pk_bf16_f32 v103, v64, v65
	v_cvt_pk_bf16_f32 v104, v66, v67
	s_lshl_b32 s31, s29, 14
	v_add_u32_e32 v182, s31, v253
	ds_read_b64_tr_b16 v[64:65], v182 offset:0
	ds_read_b64_tr_b16 v[66:67], v182 offset:0x100
	v_add_f32_e32 v68, v105, v68
	v_add_f32_e32 v68, v106, v68
	v_add_f32_e32 v68, v107, v68
	v_add_f32_e32 v68, v72, v68
	v_add_f32_e32 v68, v73, v68
	v_add_f32_e32 v215, v74, v68
	ds_read_b64_tr_b16 v[68:69], v182 offset:0x1000
	ds_read_b64_tr_b16 v[70:71], v182 offset:0x1100
	v_cvt_pk_bf16_f32 v108, v173, v175
	v_cvt_pk_bf16_f32 v109, v171, v174
	v_cvt_pk_bf16_f32 v110, v169, v172
	v_cvt_pk_bf16_f32 v111, v168, v170
	v_cvt_pk_bf16_f32 v101, v217, v218
	v_cvt_pk_bf16_f32 v102, v223, v232
	v_cvt_pk_bf16_f32 v105, v105, v106
	v_cvt_pk_bf16_f32 v106, v107, v72
	v_cvt_pk_bf16_f32 v107, v73, v74
	s_addc_u32 s67, s35, 0
	s_andn2_b64 vcc, exec, s[2:3]
	s_cbranch_vccnz .LBB4_777
	s_mov_b64 s[2:3], s[8:9]
	global_store_dwordx2 v193, v[184:185], s[2:3] nt
.LBB4_777:
	ds_read_b64_tr_b16 v[72:73], v182 offset:0x2000
	ds_read_b64_tr_b16 v[74:75], v182 offset:0x2100
	ds_read_b64_tr_b16 v[76:77], v182 offset:0x3000
	ds_read_b64_tr_b16 v[78:79], v182 offset:0x3100
	s_waitcnt lgkmcnt(0)
	v_mfma_f32_32x32x16_bf16 v[48:63], v[64:67], v[96:99], v[48:63]
	v_max_f32_e32 v64, v128, v129
	v_max3_f32 v64, v64, v130, v131
	v_max3_f32 v64, v64, v132, v133
	v_max3_f32 v64, v64, v134, v135
	v_max3_f32 v64, v64, v136, v137
	v_mfma_f32_32x32x16_bf16 v[48:63], v[68:71], v[108:111], v[48:63]
	v_max3_f32 v64, v64, v138, v139
	v_max3_f32 v66, v64, v140, v141
	ds_read_b64_tr_b16 v[64:65], v182 offset:0x200
	v_max3_f32 v180, v66, v142, v143
	ds_read_b64_tr_b16 v[66:67], v182 offset:0x300
	ds_read_b64_tr_b16 v[68:69], v182 offset:0x1200
	ds_read_b64_tr_b16 v[70:71], v182 offset:0x1300
	v_mfma_f32_32x32x16_bf16 v[48:63], v[72:75], v[100:103], v[48:63]
	ds_read_b64_tr_b16 v[72:73], v182 offset:0x2200
	ds_read_b64_tr_b16 v[74:75], v182 offset:0x2300
	ds_read_b64_tr_b16 v[218:219], v182 offset:0x3200
	ds_read_b64_tr_b16 v[220:221], v182 offset:0x3300
	v_mfma_f32_32x32x16_bf16 v[48:63], v[76:79], v[104:107], v[48:63]
	s_waitcnt lgkmcnt(0)
	v_mfma_f32_32x32x16_bf16 v[32:47], v[64:67], v[96:99], v[32:47]
	v_max3_f32 v76, v180, v112, v113
	v_max3_f32 v64, v76, v114, v115
	ds_read_b64_tr_b16 v[66:67], v182 offset:0x400
	v_max3_f32 v64, v64, v116, v117
	v_max3_f32 v64, v64, v118, v119
	v_max3_f32 v64, v64, v120, v121
	v_max3_f32 v64, v64, v122, v123
	v_mfma_f32_32x32x16_bf16 v[32:47], v[68:71], v[108:111], v[32:47]
	ds_read_b64_tr_b16 v[68:69], v182 offset:0x500
	ds_read_b64_tr_b16 v[70:71], v182 offset:0x1400
	v_max3_f32 v64, v64, v124, v125
	v_max3_f32 v64, v64, v126, v127
	v_mov_b32_e32 v65, v64
	s_nop 1
	v_permlane32_swap_b32_e32 v64, v65
	v_mfma_f32_32x32x16_bf16 v[32:47], v[72:75], v[100:103], v[32:47]
	ds_read_b64_tr_b16 v[72:73], v182 offset:0x1500
	ds_read_b64_tr_b16 v[74:75], v182 offset:0x2400
	ds_read_b64_tr_b16 v[76:77], v182 offset:0x2500
	ds_read_b64_tr_b16 v[222:223], v182 offset:0x3400
	ds_read_b64_tr_b16 v[224:225], v182 offset:0x3500
	v_mfma_f32_32x32x16_bf16 v[32:47], v[218:221], v[104:107], v[32:47]
	s_waitcnt lgkmcnt(0)
	v_max_f32_e32 v64, v64, v65
	v_mfma_f32_32x32x16_bf16 v[16:31], v[66:69], v[96:99], v[16:31]
	v_cmp_ge_f32_e32 vcc, s26, v64
	s_cmp_eq_u64 vcc, exec
	v_mfma_f32_32x32x16_bf16 v[16:31], v[70:73], v[108:111], v[16:31]
	v_mfma_f32_32x32x16_bf16 v[16:31], v[74:77], v[100:103], v[16:31]
	v_mfma_f32_32x32x16_bf16 v[16:31], v[222:225], v[104:107], v[16:31]
	s_cbranch_scc0 .LBB4_810
	v_mov_b32_e32 v180, 1.0

; template <int OFF> DI s16x4 tr_read(int vb) { s16x4 r; asm volatile("ds_read_b64_tr_b16 %0, %1 offset:%2" : "=&v"(r) : "v"(vb), "i"(OFF) : "memory"); return r; }
; DI void finishSM(f32x16& p0, f32x16& p1, float alpha, float& l_reg, bf16x8& pa0, bf16x8& pa1, bf16x8& pa2, bf16x8& pa3) {
; #pragma unroll
;     for (int r = 0; r < 16; ++r) p1[r] = __builtin_amdgcn_exp2f(p1[r]);
;     float ps = 0;
; #pragma unroll
;     for (int r = 0; r < 16; ++r) ps += p0[r];
; #pragma unroll
;     for (int r = 0; r < 16; ++r) ps += p1[r];
;     { auto rr = __builtin_amdgcn_permlane32_swap(__float_as_uint(ps), __float_as_uint(ps), false, false); ps = __uint_as_float(rr[0]) + __uint_as_float(rr[1]); }
;     l_reg = l_reg * alpha + ps;
;     ...
;     AT_PK4(p0, 0, pa0); AT_PK4(p0, 8, pa1); AT_PK4(p1, 0, pa2); AT_PK4(p1, 8, pa3);
;     ...
; }
; DI void qkt(f32x16& p0, f32x16& p1, const char* Ks, const bf16x8* qr, const f32x16& negm, int r32, int hi) {
; #pragma unroll
;     for (int d0 = 0; d0 < 4; ++d0) { const int cb = (d0 * 16 + hi * 8) * 2;
;         const bf16x8 b0 = *reinterpret_cast<const bf16x8*>(Ks + AT_KSWZ(r32, cb));
;         const bf16x8 b1 = *reinterpret_cast<const bf16x8*>(Ks + AT_KSWZ(32 + r32, cb));
;         p0 = __builtin_amdgcn_mfma_f32_32x32x16_bf16(b0, qr[d0], d0 == 0 ? negm : p0, 0, 0, 0);
;         p1 = __builtin_amdgcn_mfma_f32_32x32x16_bf16(b1, qr[d0], d0 == 0 ? negm : p1, 0, 0, 0); }
; }
; template <int D0> DI void pv_one(f32x16& od, int vb, bf16x8 pa0, bf16x8 pa1, bf16x8 pa2, bf16x8 pa3) {
;     const s16x4 l0 = tr_read<v_rd_off(D0, 0, 0)>(vb), h0 = tr_read<v_rd_off(D0, 0, 1)>(vb), l1 = tr_read<v_rd_off(D0, 1, 0)>(vb), h1 = tr_read<v_rd_off(D0, 1, 1)>(vb);
;     const s16x4 l2 = tr_read<v_rd_off(D0, 2, 0)>(vb), h2 = tr_read<v_rd_off(D0, 2, 1)>(vb), l3 = tr_read<v_rd_off(D0, 3, 0)>(vb), h3 = tr_read<v_rd_off(D0, 3, 1)>(vb);
.LBB4_796:
	v_exp_f32_e32 v182, v128
	v_exp_f32_e32 v234, v129
	v_exp_f32_e32 v235, v130
	v_exp_f32_e32 v236, v131
	v_exp_f32_e32 v237, v132
	v_exp_f32_e32 v238, v133
	v_exp_f32_e32 v239, v134
	v_exp_f32_e32 v240, v135
	v_exp_f32_e32 v241, v136
	v_exp_f32_e32 v242, v137
	v_exp_f32_e32 v243, v138
	v_exp_f32_e32 v244, v139
	v_exp_f32_e32 v245, v140
	v_exp_f32_e32 v246, v141
	v_exp_f32_e32 v247, v142
	v_exp_f32_e32 v248, v143
	v_add_u32_e32 v101, s65, v208
	v_add_u32_e32 v102, s65, v209
	v_add_u32_e32 v103, s65, v210
	ds_read_b128 v[172:175], v101 offset:49152
	ds_read_b128 v[176:179], v101 offset:53248
	ds_read_b128 v[218:221], v102 offset:49152
	ds_read_b128 v[222:225], v102 offset:53248
	ds_read_b128 v[226:229], v103 offset:49152
	ds_read_b128 v[230:233], v103 offset:53248
	v_exp_f32_e32 v112, v112
	v_exp_f32_e32 v113, v113
	v_exp_f32_e32 v114, v114
	s_waitcnt lgkmcnt(7)
	v_mfma_f32_32x32x16_bf16 v[128:143], v[96:99], v[156:159], v[80:95]
	s_add_u32 s24, s34, 0x2380c000
	s_addc_u32 s25, s35, 0
	s_add_u32 s34, s34, 0x2380e000
	s_addc_u32 s35, s35, 0
	s_add_u32 s66, s37, 0x21886000
	s_addc_u32 s67, s64, 0
	s_lshl_b32 s92, s29, 14
	s_add_i32 s92, s92, s94
	s_mov_b32 m0, s92
	s_lshl_b32 s96, s29, 13
	global_load_lds_dwordx4 v249, s[24:25]
	s_addk_i32 s92, 0x400
	s_mov_b32 m0, s92
	s_add_i32 s96, s96, s95
	global_load_lds_dwordx4 v250, s[24:25]
	s_nop 0
	s_mov_b32 m0, s96
	s_nop 0
	global_load_lds_dwordx4 v251, s[66:67]
	s_nop 0
	v_exp_f32_e32 v115, v115
	v_exp_f32_e32 v116, v116
	v_exp_f32_e32 v117, v117
	v_exp_f32_e32 v118, v118
	v_exp_f32_e32 v119, v119
	s_waitcnt lgkmcnt(6)
	v_mfma_f32_32x32x16_bf16 v[96:111], v[168:171], v[156:159], v[80:95]
	v_exp_f32_e32 v168, v120
	v_add_f32_e32 v120, 0, v182
	v_add_f32_e32 v120, v234, v120
	v_add_f32_e32 v120, v235, v120
	v_add_f32_e32 v120, v236, v120
	v_add_f32_e32 v120, v237, v120
	v_add_f32_e32 v120, v238, v120
	v_add_f32_e32 v120, v239, v120
	v_add_f32_e32 v120, v240, v120
	v_add_f32_e32 v120, v241, v120
	v_add_f32_e32 v120, v242, v120
	s_waitcnt lgkmcnt(5)
	v_mfma_f32_32x32x16_bf16 v[128:143], v[172:175], v[152:155], v[128:143]
	v_add_f32_e32 v120, v243, v120
	v_add_f32_e32 v120, v244, v120
	v_add_f32_e32 v120, v245, v120
	v_add_f32_e32 v120, v246, v120
	v_add_f32_e32 v120, v247, v120
	v_add_f32_e32 v120, v248, v120
	v_add_f32_e32 v120, v112, v120
	s_waitcnt lgkmcnt(4)
	v_mfma_f32_32x32x16_bf16 v[96:111], v[176:179], v[152:155], v[96:111]
	v_add_f32_e32 v120, v113, v120
	v_add_f32_e32 v120, v114, v120
	v_add_f32_e32 v120, v115, v120
	v_add_f32_e32 v120, v116, v120
	v_exp_f32_e32 v169, v121
	v_add_f32_e32 v120, v117, v120
	v_exp_f32_e32 v170, v122
	s_waitcnt lgkmcnt(3)
	v_mfma_f32_32x32x16_bf16 v[128:143], v[218:221], v[148:151], v[128:143]
	v_add_f32_e32 v120, v118, v120
	v_exp_f32_e32 v171, v123
	v_add_f32_e32 v120, v119, v120
	v_exp_f32_e32 v172, v124
	v_add_f32_e32 v120, v168, v120
	v_exp_f32_e32 v173, v125
	v_add_f32_e32 v120, v169, v120
	s_waitcnt lgkmcnt(2)
	v_mfma_f32_32x32x16_bf16 v[96:111], v[222:225], v[148:151], v[96:111]
	v_exp_f32_e32 v174, v126
	v_add_f32_e32 v120, v170, v120
	v_exp_f32_e32 v175, v127
	v_add_f32_e32 v120, v171, v120
	v_add_f32_e32 v120, v172, v120
	v_add_f32_e32 v120, v173, v120
	v_add_f32_e32 v120, v174, v120
	s_waitcnt lgkmcnt(1)
	v_mfma_f32_32x32x16_bf16 v[128:143], v[226:229], v[144:147], v[128:143]
	v_add_f32_e32 v217, v175, v120
	v_cvt_pk_bf16_f32 v120, v182, v234
	v_cvt_pk_bf16_f32 v121, v235, v236
	v_cvt_pk_bf16_f32 v122, v237, v238
	v_cvt_pk_bf16_f32 v123, v239, v240
	v_cvt_pk_bf16_f32 v124, v241, v242
	s_waitcnt lgkmcnt(0)
	v_mfma_f32_32x32x16_bf16 v[96:111], v[230:233], v[144:147], v[96:111]
	v_lshl_add_u32 v219, s30, 14, v253
	ds_read_b64_tr_b16 v[220:221], v219 offset:0
	ds_read_b64_tr_b16 v[222:223], v219 offset:0x100
	ds_read_b64_tr_b16 v[224:225], v219 offset:0x1000
	ds_read_b64_tr_b16 v[226:227], v219 offset:0x1100
	v_cvt_pk_bf16_f32 v125, v243, v244
	v_cvt_pk_bf16_f32 v126, v245, v246
	v_cvt_pk_bf16_f32 v127, v247, v248
	v_cvt_pk_bf16_f32 v112, v112, v113
	v_cvt_pk_bf16_f32 v113, v114, v115
	v_cvt_pk_bf16_f32 v114, v116, v117
	v_cvt_pk_bf16_f32 v115, v118, v119
	v_cvt_pk_bf16_f32 v116, v168, v169
	v_cvt_pk_bf16_f32 v117, v170, v171
	v_cvt_pk_bf16_f32 v118, v172, v173
	v_cvt_pk_bf16_f32 v119, v174, v175
	s_and_b64 vcc, exec, s[2:3]
	s_cbranch_vccnz .LBB4_798
	s_mov_b64 s[2:3], s[8:9]
	global_store_dwordx2 v193, v[184:185], s[2:3] nt
; #define AT_SBAR() __builtin_amdgcn_sched_barrier(0)
; template <int OFF> DI s16x4 tr_read(int vb) { s16x4 r; asm volatile("ds_read_b64_tr_b16 %0, %1 offset:%2" : "=&v"(r) : "v"(vb), "i"(OFF) : "memory"); return r; }
; template <int D0> DI void pv_one(f32x16& od, int vb, bf16x8 pa0, bf16x8 pa1, bf16x8 pa2, bf16x8 pa3) {
;     const s16x4 l0 = tr_read<v_rd_off(D0, 0, 0)>(vb), h0 = tr_read<v_rd_off(D0, 0, 1)>(vb), l1 = tr_read<v_rd_off(D0, 1, 0)>(vb), h1 = tr_read<v_rd_off(D0, 1, 1)>(vb);
;     const s16x4 l2 = tr_read<v_rd_off(D0, 2, 0)>(vb), h2 = tr_read<v_rd_off(D0, 2, 1)>(vb), l3 = tr_read<v_rd_off(D0, 3, 0)>(vb), h3 = tr_read<v_rd_off(D0, 3, 1)>(vb);
;     asm volatile("s_waitcnt lgkmcnt(0)" ::: "memory"); AT_SBAR();
;     ...
;     od = __builtin_amdgcn_mfma_f32_32x32x16_bf16(AT_PK(l0, h0), pa0, od, 0, 0, 0);
;     od = __builtin_amdgcn_mfma_f32_32x32x16_bf16(AT_PK(l1, h1), pa1, od, 0, 0, 0);
;     od = __builtin_amdgcn_mfma_f32_32x32x16_bf16(AT_PK(l2, h2), pa2, od, 0, 0, 0);
;     od = __builtin_amdgcn_mfma_f32_32x32x16_bf16(AT_PK(l3, h3), pa3, od, 0, 0, 0);
;     ...
; }
; DI void pv_all_sm(f32x16* o, int vb, bf16x8 pa0, bf16x8 pa1, bf16x8 pa2, bf16x8 pa3, f32x16& p0, f32x16& p1, float& m_ref, f32x16& negm, float& alpha) {
;     pv_one<0>(o[0], vb, pa0, pa1, pa2, pa3);
;     float pmax = p0[0];
; #pragma unroll
;     for (int r = 1; r < 16; ++r) pmax = fmaxf(pmax, p0[r]);
;     pv_one<1>(o[1], vb, pa0, pa1, pa2, pa3);
; #pragma unroll
;     for (int r = 0; r < 16; ++r) pmax = fmaxf(pmax, p1[r]);
;     { auto rr = __builtin_amdgcn_permlane32_swap(__float_as_uint(pmax), __float_as_uint(pmax), false, false); pmax = fmaxf(__uint_as_float(rr[0]), __uint_as_float(rr[1])); }
;     pv_one<2>(o[2], vb, pa0, pa1, pa2, pa3);
;     alpha = 1.f;
;     if (__builtin_expect(!__all(pmax <= THRL), 0)) {
.LBB4_798:
	ds_read_b64_tr_b16 v[228:229], v219 offset:0x2000
	ds_read_b64_tr_b16 v[230:231], v219 offset:0x2100
	ds_read_b64_tr_b16 v[232:233], v219 offset:0x3000
	ds_read_b64_tr_b16 v[234:235], v219 offset:0x3100
	s_waitcnt lgkmcnt(0)
	v_mfma_f32_32x32x16_bf16 v[48:63], v[220:223], v[120:123], v[48:63]
	v_max_f32_e32 v182, v128, v129
	ds_read_b64_tr_b16 v[220:221], v219 offset:0x200
	ds_read_b64_tr_b16 v[222:223], v219 offset:0x300
	v_max3_f32 v182, v182, v130, v131
	v_max3_f32 v182, v182, v132, v133
	v_mfma_f32_32x32x16_bf16 v[48:63], v[224:227], v[124:127], v[48:63]
	ds_read_b64_tr_b16 v[224:225], v219 offset:0x1200
	ds_read_b64_tr_b16 v[226:227], v219 offset:0x1300
	v_max3_f32 v182, v182, v134, v135
	v_max3_f32 v182, v182, v136, v137
	v_max3_f32 v182, v182, v138, v139
	v_max3_f32 v182, v182, v140, v141
	v_max3_f32 v182, v182, v142, v143
	v_mfma_f32_32x32x16_bf16 v[48:63], v[228:231], v[112:115], v[48:63]
	ds_read_b64_tr_b16 v[228:229], v219 offset:0x2200
	ds_read_b64_tr_b16 v[230:231], v219 offset:0x2300
	ds_read_b64_tr_b16 v[236:237], v219 offset:0x3200
	ds_read_b64_tr_b16 v[238:239], v219 offset:0x3300
	v_mfma_f32_32x32x16_bf16 v[48:63], v[232:235], v[116:119], v[48:63]
	s_waitcnt lgkmcnt(0)
	v_mfma_f32_32x32x16_bf16 v[32:47], v[220:223], v[120:123], v[32:47]
	v_max3_f32 v182, v182, v96, v97
	v_max3_f32 v182, v182, v98, v99
	ds_read_b64_tr_b16 v[222:223], v219 offset:0x400
	v_max3_f32 v182, v182, v100, v101
	v_max3_f32 v182, v182, v102, v103
	v_max3_f32 v182, v182, v104, v105
	v_max3_f32 v182, v182, v106, v107
	v_mfma_f32_32x32x16_bf16 v[32:47], v[224:227], v[124:127], v[32:47]
	ds_read_b64_tr_b16 v[224:225], v219 offset:0x500
	ds_read_b64_tr_b16 v[226:227], v219 offset:0x1400
	v_max3_f32 v182, v182, v108, v109
	v_max3_f32 v182, v182, v110, v111
	v_mov_b32_e32 v220, v182
	s_nop 1
	v_permlane32_swap_b32_e32 v182, v220
	v_mfma_f32_32x32x16_bf16 v[32:47], v[228:231], v[112:115], v[32:47]
	ds_read_b64_tr_b16 v[228:229], v219 offset:0x1500
	ds_read_b64_tr_b16 v[230:231], v219 offset:0x2400
	ds_read_b64_tr_b16 v[232:233], v219 offset:0x2500
	ds_read_b64_tr_b16 v[240:241], v219 offset:0x3400
	ds_read_b64_tr_b16 v[242:243], v219 offset:0x3500
	v_mfma_f32_32x32x16_bf16 v[32:47], v[236:239], v[116:119], v[32:47]
	s_waitcnt lgkmcnt(0)
	v_max_f32_e32 v220, v182, v220
	v_mfma_f32_32x32x16_bf16 v[16:31], v[222:225], v[120:123], v[16:31]
	v_cmp_ge_f32_e32 vcc, s26, v220
	s_cmp_eq_u64 vcc, exec
	v_mov_b32_e32 v182, 1.0
	v_mfma_f32_32x32x16_bf16 v[16:31], v[226:229], v[124:127], v[16:31]
	v_mfma_f32_32x32x16_bf16 v[16:31], v[230:233], v[112:115], v[16:31]
	v_mfma_f32_32x32x16_bf16 v[16:31], v[240:243], v[116:119], v[16:31]
	s_cbranch_scc0 .LBB4_811

; DI void finishSM(f32x16& p0, f32x16& p1, float alpha, float& l_reg, bf16x8& pa0, bf16x8& pa1, bf16x8& pa2, bf16x8& pa3) {
; #pragma unroll
;     for (int r = 0; r < 16; ++r) p1[r] = __builtin_amdgcn_exp2f(p1[r]);
;     float ps = 0;
; #pragma unroll
;     for (int r = 0; r < 16; ++r) ps += p0[r];
; #pragma unroll
;     for (int r = 0; r < 16; ++r) ps += p1[r];
;     { auto rr = __builtin_amdgcn_permlane32_swap(__float_as_uint(ps), __float_as_uint(ps), false, false); ps = __uint_as_float(rr[0]) + __uint_as_float(rr[1]); }
;     l_reg = l_reg * alpha + ps;
;     ...
;     AT_PK4(p0, 0, pa0); AT_PK4(p0, 8, pa1); AT_PK4(p1, 0, pa2); AT_PK4(p1, 8, pa3);
;     ...
; }
; DI void qkt(f32x16& p0, f32x16& p1, const char* Ks, const bf16x8* qr, const f32x16& negm, int r32, int hi) {
; #pragma unroll
;     for (int d0 = 0; d0 < 4; ++d0) { const int cb = (d0 * 16 + hi * 8) * 2;
;         const bf16x8 b0 = *reinterpret_cast<const bf16x8*>(Ks + AT_KSWZ(r32, cb));
;         const bf16x8 b1 = *reinterpret_cast<const bf16x8*>(Ks + AT_KSWZ(32 + r32, cb));
;         p0 = __builtin_amdgcn_mfma_f32_32x32x16_bf16(b0, qr[d0], d0 == 0 ? negm : p0, 0, 0, 0);
;         p1 = __builtin_amdgcn_mfma_f32_32x32x16_bf16(b1, qr[d0], d0 == 0 ? negm : p1, 0, 0, 0); }
; }
; DI void pv_all_sm(f32x16* o, int vb, bf16x8 pa0, bf16x8 pa1, bf16x8 pa2, bf16x8 pa3, f32x16& p0, f32x16& p1, float& m_ref, f32x16& negm, float& alpha) {
;     pv_one<0>(o[0], vb, pa0, pa1, pa2, pa3);
;     float pmax = p0[0];
; #pragma unroll
;     for (int r = 1; r < 16; ++r) pmax = fmaxf(pmax, p0[r]);
;     pv_one<1>(o[1], vb, pa0, pa1, pa2, pa3);
; #pragma unroll
;     for (int r = 0; r < 16; ++r) pmax = fmaxf(pmax, p1[r]);
;     { auto rr = __builtin_amdgcn_permlane32_swap(__float_as_uint(pmax), __float_as_uint(pmax), false, false); pmax = fmaxf(__uint_as_float(rr[0]), __uint_as_float(rr[1])); }
;     pv_one<2>(o[2], vb, pa0, pa1, pa2, pa3);
;     alpha = 1.f;
;     if (__builtin_expect(!__all(pmax <= THRL), 0)) {
.LBB4_849:
	s_lshl_b32 s26, s64, 13
	s_add_i32 s26, s26, 0
	v_add_u32_e32 v72, s26, v204
	v_add_u32_e32 v112, s26, v205
	v_add_u32_e32 v180, s26, v206
	s_waitcnt lgkmcnt(1)
	v_mfma_f32_32x32x16_bf16 v[128:143], v[64:67], v[156:159], v[80:95]
	ds_read_b128 v[64:67], v72 offset:49152
	ds_read_b128 v[72:75], v72 offset:53248
	ds_read_b128 v[76:79], v112 offset:49152
	ds_read_b128 v[220:223], v112 offset:53248
	s_add_u32 s66, s46, s28
	s_addc_u32 s67, s47, s29
	s_add_u32 s34, s66, 0x23808000
	s_addc_u32 s35, s67, 0
	s_add_u32 s76, s66, 0x2380a000
	s_add_u32 s74, s46, s24
	s_addc_u32 s75, s47, s25
	s_add_u32 s78, s74, 0x21804000
	s_addc_u32 s79, s75, 0
	s_lshl_b32 s92, s57, 14
	s_add_i32 s92, s92, s94
	s_mov_b32 m0, s92
	s_lshl_b32 s96, s57, 13
	global_load_lds_dwordx4 v249, s[34:35]
	s_addk_i32 s92, 0x400
	s_mov_b32 m0, s92
	s_add_i32 s96, s96, s95
	global_load_lds_dwordx4 v250, s[34:35]
	s_nop 0
	s_mov_b32 m0, s96
	s_nop 0
	global_load_lds_dwordx4 v251, s[78:79]
	v_exp_f32_e32 v182, v97
	v_exp_f32_e32 v213, v98
	v_exp_f32_e32 v214, v99
	v_exp_f32_e32 v219, v100
	v_exp_f32_e32 v228, v101
	s_waitcnt lgkmcnt(4)
	v_mfma_f32_32x32x16_bf16 v[112:127], v[68:71], v[156:159], v[80:95]
	ds_read_b128 v[68:71], v180 offset:49152
	ds_read_b128 v[224:227], v180 offset:53248
	v_exp_f32_e32 v180, v96
	v_cvt_pk_bf16_f32 v96, v216, v218
	v_cvt_pk_bf16_f32 v97, v179, v217
	v_cvt_pk_bf16_f32 v98, v177, v215
	v_cvt_pk_bf16_f32 v99, v176, v178
	s_waitcnt lgkmcnt(4)
	v_mfma_f32_32x32x16_bf16 v[112:127], v[72:75], v[152:155], v[112:127]
	v_add_f32_e32 v75, 0, v216
	v_add_f32_e32 v75, v218, v75
	v_add_f32_e32 v75, v179, v75
	v_add_f32_e32 v75, v217, v75
	v_add_f32_e32 v75, v177, v75
	v_add_f32_e32 v75, v215, v75
	v_add_f32_e32 v75, v176, v75
	v_mfma_f32_32x32x16_bf16 v[128:143], v[64:67], v[152:155], v[128:143]
	v_add_f32_e32 v75, v178, v75
	v_add_f32_e32 v75, v173, v75
	v_add_f32_e32 v75, v175, v75
	v_add_f32_e32 v75, v171, v75
	v_add_f32_e32 v75, v174, v75
	v_add_f32_e32 v75, v169, v75
	v_add_f32_e32 v75, v172, v75
	s_waitcnt lgkmcnt(3)
	v_mfma_f32_32x32x16_bf16 v[128:143], v[76:79], v[148:151], v[128:143]
	v_add_f32_e32 v75, v168, v75
	v_add_f32_e32 v75, v170, v75
	v_add_f32_e32 v75, v180, v75
	v_add_f32_e32 v75, v182, v75
	v_exp_f32_e32 v64, v102
	v_exp_f32_e32 v65, v103
	v_exp_f32_e32 v66, v104
	s_waitcnt lgkmcnt(2)
	v_mfma_f32_32x32x16_bf16 v[112:127], v[220:223], v[148:151], v[112:127]
	v_exp_f32_e32 v67, v105
	v_exp_f32_e32 v105, v106
	v_exp_f32_e32 v106, v107
	v_exp_f32_e32 v107, v108
	v_exp_f32_e32 v72, v109
	v_exp_f32_e32 v73, v110
	v_exp_f32_e32 v74, v111
	s_waitcnt lgkmcnt(1)
	v_mfma_f32_32x32x16_bf16 v[128:143], v[68:71], v[144:147], v[128:143]
	v_add_f32_e32 v68, v213, v75
	v_add_f32_e32 v68, v214, v68
	v_add_f32_e32 v68, v219, v68
	v_add_f32_e32 v68, v228, v68
	v_add_f32_e32 v68, v64, v68
	v_add_f32_e32 v68, v65, v68
	v_add_f32_e32 v68, v66, v68
	v_add_f32_e32 v68, v67, v68
	s_waitcnt lgkmcnt(0)
	v_mfma_f32_32x32x16_bf16 v[112:127], v[224:227], v[144:147], v[112:127]
	v_cvt_pk_bf16_f32 v100, v180, v182
	v_cvt_pk_bf16_f32 v103, v64, v65
	v_cvt_pk_bf16_f32 v104, v66, v67
	s_lshl_b32 s65, s63, 14
	v_add_u32_e32 v182, s65, v253
	ds_read_b64_tr_b16 v[64:65], v182 offset:0
	ds_read_b64_tr_b16 v[66:67], v182 offset:0x100
	v_add_f32_e32 v68, v105, v68
	v_add_f32_e32 v68, v106, v68
	v_add_f32_e32 v68, v107, v68
	v_add_f32_e32 v68, v72, v68
	v_add_f32_e32 v68, v73, v68
	v_add_f32_e32 v211, v74, v68
	ds_read_b64_tr_b16 v[68:69], v182 offset:0x1000
	ds_read_b64_tr_b16 v[70:71], v182 offset:0x1100
	v_cvt_pk_bf16_f32 v108, v173, v175
	v_cvt_pk_bf16_f32 v109, v171, v174
	v_cvt_pk_bf16_f32 v110, v169, v172
	v_cvt_pk_bf16_f32 v111, v168, v170
	v_cvt_pk_bf16_f32 v101, v213, v214
	v_cvt_pk_bf16_f32 v102, v219, v228
	v_cvt_pk_bf16_f32 v105, v105, v106
	v_cvt_pk_bf16_f32 v106, v107, v72
	v_cvt_pk_bf16_f32 v107, v73, v74
	s_addc_u32 s77, s67, 0
	s_andn2_b64 vcc, exec, s[2:3]
	s_cbranch_vccnz .LBB4_851
	s_mov_b64 s[2:3], s[8:9]
	global_store_dwordx2 v188, v[184:185], s[2:3] nt
.LBB4_851:
	ds_read_b64_tr_b16 v[72:73], v182 offset:0x2000
	ds_read_b64_tr_b16 v[74:75], v182 offset:0x2100
	ds_read_b64_tr_b16 v[76:77], v182 offset:0x3000
	ds_read_b64_tr_b16 v[78:79], v182 offset:0x3100
	s_waitcnt lgkmcnt(0)
	v_mfma_f32_32x32x16_bf16 v[32:47], v[64:67], v[96:99], v[32:47]
	v_max_f32_e32 v64, v128, v129
	v_max3_f32 v64, v64, v130, v131
	v_max3_f32 v64, v64, v132, v133
	v_max3_f32 v64, v64, v134, v135
	v_max3_f32 v64, v64, v136, v137
	v_mfma_f32_32x32x16_bf16 v[32:47], v[68:71], v[108:111], v[32:47]
	v_max3_f32 v64, v64, v138, v139
	v_max3_f32 v66, v64, v140, v141
	ds_read_b64_tr_b16 v[64:65], v182 offset:0x200
	v_max3_f32 v180, v66, v142, v143
	ds_read_b64_tr_b16 v[66:67], v182 offset:0x300
	ds_read_b64_tr_b16 v[68:69], v182 offset:0x1200
	ds_read_b64_tr_b16 v[70:71], v182 offset:0x1300
	v_mfma_f32_32x32x16_bf16 v[32:47], v[72:75], v[100:103], v[32:47]
	ds_read_b64_tr_b16 v[72:73], v182 offset:0x2200
	ds_read_b64_tr_b16 v[74:75], v182 offset:0x2300
	ds_read_b64_tr_b16 v[214:215], v182 offset:0x3200
	ds_read_b64_tr_b16 v[216:217], v182 offset:0x3300
	v_mfma_f32_32x32x16_bf16 v[32:47], v[76:79], v[104:107], v[32:47]
	s_waitcnt lgkmcnt(0)
	v_mfma_f32_32x32x16_bf16 v[48:63], v[64:67], v[96:99], v[48:63]
	v_max3_f32 v76, v180, v112, v113
	v_max3_f32 v64, v76, v114, v115
	ds_read_b64_tr_b16 v[66:67], v182 offset:0x400
	v_max3_f32 v64, v64, v116, v117
	v_max3_f32 v64, v64, v118, v119
	v_max3_f32 v64, v64, v120, v121
	v_max3_f32 v64, v64, v122, v123
	v_mfma_f32_32x32x16_bf16 v[48:63], v[68:71], v[108:111], v[48:63]
	ds_read_b64_tr_b16 v[68:69], v182 offset:0x500
	ds_read_b64_tr_b16 v[70:71], v182 offset:0x1400
	v_max3_f32 v64, v64, v124, v125
	v_max3_f32 v64, v64, v126, v127
	v_mov_b32_e32 v65, v64
	s_nop 1
	v_permlane32_swap_b32_e32 v64, v65
	v_mfma_f32_32x32x16_bf16 v[48:63], v[72:75], v[100:103], v[48:63]
	ds_read_b64_tr_b16 v[72:73], v182 offset:0x1500
	ds_read_b64_tr_b16 v[74:75], v182 offset:0x2400
	ds_read_b64_tr_b16 v[76:77], v182 offset:0x2500
	ds_read_b64_tr_b16 v[218:219], v182 offset:0x3400
	ds_read_b64_tr_b16 v[220:221], v182 offset:0x3500
	v_mfma_f32_32x32x16_bf16 v[48:63], v[214:217], v[104:107], v[48:63]
	s_waitcnt lgkmcnt(0)
	v_max_f32_e32 v64, v64, v65
	v_mfma_f32_32x32x16_bf16 v[16:31], v[66:69], v[96:99], v[16:31]
	v_cmp_ge_f32_e32 vcc, s15, v64
	s_cmp_eq_u64 vcc, exec
	v_mfma_f32_32x32x16_bf16 v[16:31], v[70:73], v[108:111], v[16:31]
	v_mfma_f32_32x32x16_bf16 v[16:31], v[74:77], v[100:103], v[16:31]
	v_mfma_f32_32x32x16_bf16 v[16:31], v[218:221], v[104:107], v[16:31]
	s_cbranch_scc0 .LBB4_884
	v_mov_b32_e32 v180, 1.0

; template <int OFF> DI s16x4 tr_read(int vb) { s16x4 r; asm volatile("ds_read_b64_tr_b16 %0, %1 offset:%2" : "=&v"(r) : "v"(vb), "i"(OFF) : "memory"); return r; }
; DI void finishSM(f32x16& p0, f32x16& p1, float alpha, float& l_reg, bf16x8& pa0, bf16x8& pa1, bf16x8& pa2, bf16x8& pa3) {
; #pragma unroll
;     for (int r = 0; r < 16; ++r) p1[r] = __builtin_amdgcn_exp2f(p1[r]);
;     float ps = 0;
; #pragma unroll
;     for (int r = 0; r < 16; ++r) ps += p0[r];
; #pragma unroll
;     for (int r = 0; r < 16; ++r) ps += p1[r];
;     { auto rr = __builtin_amdgcn_permlane32_swap(__float_as_uint(ps), __float_as_uint(ps), false, false); ps = __uint_as_float(rr[0]) + __uint_as_float(rr[1]); }
;     l_reg = l_reg * alpha + ps;
;     ...
;     AT_PK4(p0, 0, pa0); AT_PK4(p0, 8, pa1); AT_PK4(p1, 0, pa2); AT_PK4(p1, 8, pa3);
;     ...
; }
; DI void qkt(f32x16& p0, f32x16& p1, const char* Ks, const bf16x8* qr, const f32x16& negm, int r32, int hi) {
; #pragma unroll
;     for (int d0 = 0; d0 < 4; ++d0) { const int cb = (d0 * 16 + hi * 8) * 2;
;         const bf16x8 b0 = *reinterpret_cast<const bf16x8*>(Ks + AT_KSWZ(r32, cb));
;         const bf16x8 b1 = *reinterpret_cast<const bf16x8*>(Ks + AT_KSWZ(32 + r32, cb));
;         p0 = __builtin_amdgcn_mfma_f32_32x32x16_bf16(b0, qr[d0], d0 == 0 ? negm : p0, 0, 0, 0);
;         p1 = __builtin_amdgcn_mfma_f32_32x32x16_bf16(b1, qr[d0], d0 == 0 ? negm : p1, 0, 0, 0); }
; }
; template <int D0> DI void pv_one(f32x16& od, int vb, bf16x8 pa0, bf16x8 pa1, bf16x8 pa2, bf16x8 pa3) {
;     const s16x4 l0 = tr_read<v_rd_off(D0, 0, 0)>(vb), h0 = tr_read<v_rd_off(D0, 0, 1)>(vb), l1 = tr_read<v_rd_off(D0, 1, 0)>(vb), h1 = tr_read<v_rd_off(D0, 1, 1)>(vb);
;     const s16x4 l2 = tr_read<v_rd_off(D0, 2, 0)>(vb), h2 = tr_read<v_rd_off(D0, 2, 1)>(vb), l3 = tr_read<v_rd_off(D0, 3, 0)>(vb), h3 = tr_read<v_rd_off(D0, 3, 1)>(vb);
.LBB4_870:
	v_exp_f32_e32 v182, v128
	v_exp_f32_e32 v230, v129
	v_exp_f32_e32 v231, v130
	v_exp_f32_e32 v232, v131
	v_exp_f32_e32 v233, v132
	v_exp_f32_e32 v234, v133
	v_exp_f32_e32 v235, v134
	v_exp_f32_e32 v236, v135
	v_exp_f32_e32 v237, v136
	v_exp_f32_e32 v238, v137
	v_exp_f32_e32 v239, v138
	v_exp_f32_e32 v240, v139
	v_exp_f32_e32 v241, v140
	v_exp_f32_e32 v242, v141
	v_exp_f32_e32 v243, v142
	v_exp_f32_e32 v244, v143
	v_add_u32_e32 v101, s76, v204
	v_add_u32_e32 v102, s76, v205
	v_add_u32_e32 v103, s76, v206
	ds_read_b128 v[172:175], v101 offset:49152
	ds_read_b128 v[176:179], v101 offset:53248
	ds_read_b128 v[214:217], v102 offset:49152
	ds_read_b128 v[218:221], v102 offset:53248
	ds_read_b128 v[222:225], v103 offset:49152
	ds_read_b128 v[226:229], v103 offset:53248
	v_exp_f32_e32 v112, v112
	v_exp_f32_e32 v113, v113
	v_exp_f32_e32 v114, v114
	s_waitcnt lgkmcnt(7)
	v_mfma_f32_32x32x16_bf16 v[128:143], v[96:99], v[156:159], v[80:95]
	s_add_u32 s34, s66, 0x2380c000
	s_addc_u32 s35, s67, 0
	s_add_u32 s66, s66, 0x2380e000
	s_addc_u32 s67, s67, 0
	s_add_u32 s74, s74, 0x21806000
	s_addc_u32 s75, s75, 0
	s_lshl_b32 s92, s63, 14
	s_add_i32 s92, s92, s94
	s_mov_b32 m0, s92
	s_lshl_b32 s96, s63, 13
	global_load_lds_dwordx4 v249, s[34:35]
	s_addk_i32 s92, 0x400
	s_mov_b32 m0, s92
	s_add_i32 s96, s96, s95
	global_load_lds_dwordx4 v250, s[34:35]
	s_nop 0
	s_mov_b32 m0, s96
	s_nop 0
	global_load_lds_dwordx4 v251, s[74:75]
	s_nop 0
	v_exp_f32_e32 v115, v115
	v_exp_f32_e32 v116, v116
	v_exp_f32_e32 v117, v117
	v_exp_f32_e32 v118, v118
	v_exp_f32_e32 v119, v119
	s_waitcnt lgkmcnt(6)
	v_mfma_f32_32x32x16_bf16 v[96:111], v[168:171], v[156:159], v[80:95]
	v_exp_f32_e32 v168, v120
	v_add_f32_e32 v120, 0, v182
	v_add_f32_e32 v120, v230, v120
	v_add_f32_e32 v120, v231, v120
	v_add_f32_e32 v120, v232, v120
	v_add_f32_e32 v120, v233, v120
	v_add_f32_e32 v120, v234, v120
	v_add_f32_e32 v120, v235, v120
	v_add_f32_e32 v120, v236, v120
	v_add_f32_e32 v120, v237, v120
	v_add_f32_e32 v120, v238, v120
	s_waitcnt lgkmcnt(5)
	v_mfma_f32_32x32x16_bf16 v[128:143], v[172:175], v[152:155], v[128:143]
	v_add_f32_e32 v120, v239, v120
	v_add_f32_e32 v120, v240, v120
	v_add_f32_e32 v120, v241, v120
	v_add_f32_e32 v120, v242, v120
	v_add_f32_e32 v120, v243, v120
	v_add_f32_e32 v120, v244, v120
	v_add_f32_e32 v120, v112, v120
	s_waitcnt lgkmcnt(4)
	v_mfma_f32_32x32x16_bf16 v[96:111], v[176:179], v[152:155], v[96:111]
	v_add_f32_e32 v120, v113, v120
	v_add_f32_e32 v120, v114, v120
	v_add_f32_e32 v120, v115, v120
	v_add_f32_e32 v120, v116, v120
	v_exp_f32_e32 v169, v121
	v_add_f32_e32 v120, v117, v120
	v_exp_f32_e32 v170, v122
	s_waitcnt lgkmcnt(3)
	v_mfma_f32_32x32x16_bf16 v[128:143], v[214:217], v[148:151], v[128:143]
	v_add_f32_e32 v120, v118, v120
	v_exp_f32_e32 v171, v123
	v_add_f32_e32 v120, v119, v120
	v_exp_f32_e32 v172, v124
	v_add_f32_e32 v120, v168, v120
	v_exp_f32_e32 v173, v125
	v_add_f32_e32 v120, v169, v120
	s_waitcnt lgkmcnt(2)
	v_mfma_f32_32x32x16_bf16 v[96:111], v[218:221], v[148:151], v[96:111]
	v_exp_f32_e32 v174, v126
	v_add_f32_e32 v120, v170, v120
	v_exp_f32_e32 v175, v127
	v_add_f32_e32 v120, v171, v120
	v_add_f32_e32 v120, v172, v120
	v_add_f32_e32 v120, v173, v120
	v_add_f32_e32 v120, v174, v120
	s_waitcnt lgkmcnt(1)
	v_mfma_f32_32x32x16_bf16 v[128:143], v[222:225], v[144:147], v[128:143]
	v_add_f32_e32 v213, v175, v120
	v_cvt_pk_bf16_f32 v120, v182, v230
	v_cvt_pk_bf16_f32 v121, v231, v232
	v_cvt_pk_bf16_f32 v122, v233, v234
	v_cvt_pk_bf16_f32 v123, v235, v236
	v_cvt_pk_bf16_f32 v124, v237, v238
	s_waitcnt lgkmcnt(0)
	v_mfma_f32_32x32x16_bf16 v[96:111], v[226:229], v[144:147], v[96:111]
	v_lshl_add_u32 v215, s64, 14, v253
	ds_read_b64_tr_b16 v[216:217], v215 offset:0
	ds_read_b64_tr_b16 v[218:219], v215 offset:0x100
	ds_read_b64_tr_b16 v[220:221], v215 offset:0x1000
	ds_read_b64_tr_b16 v[222:223], v215 offset:0x1100
	v_cvt_pk_bf16_f32 v125, v239, v240
	v_cvt_pk_bf16_f32 v126, v241, v242
	v_cvt_pk_bf16_f32 v127, v243, v244
	v_cvt_pk_bf16_f32 v112, v112, v113
	v_cvt_pk_bf16_f32 v113, v114, v115
	v_cvt_pk_bf16_f32 v114, v116, v117
	v_cvt_pk_bf16_f32 v115, v118, v119
	v_cvt_pk_bf16_f32 v116, v168, v169
	v_cvt_pk_bf16_f32 v117, v170, v171
	v_cvt_pk_bf16_f32 v118, v172, v173
	v_cvt_pk_bf16_f32 v119, v174, v175
	s_and_b64 vcc, exec, s[2:3]
	s_cbranch_vccnz .LBB4_872
	s_mov_b64 s[2:3], s[8:9]
	global_store_dwordx2 v188, v[184:185], s[2:3] nt
; #define AT_SBAR() __builtin_amdgcn_sched_barrier(0)
; template <int OFF> DI s16x4 tr_read(int vb) { s16x4 r; asm volatile("ds_read_b64_tr_b16 %0, %1 offset:%2" : "=&v"(r) : "v"(vb), "i"(OFF) : "memory"); return r; }
; template <int D0> DI void pv_one(f32x16& od, int vb, bf16x8 pa0, bf16x8 pa1, bf16x8 pa2, bf16x8 pa3) {
;     const s16x4 l0 = tr_read<v_rd_off(D0, 0, 0)>(vb), h0 = tr_read<v_rd_off(D0, 0, 1)>(vb), l1 = tr_read<v_rd_off(D0, 1, 0)>(vb), h1 = tr_read<v_rd_off(D0, 1, 1)>(vb);
;     const s16x4 l2 = tr_read<v_rd_off(D0, 2, 0)>(vb), h2 = tr_read<v_rd_off(D0, 2, 1)>(vb), l3 = tr_read<v_rd_off(D0, 3, 0)>(vb), h3 = tr_read<v_rd_off(D0, 3, 1)>(vb);
;     asm volatile("s_waitcnt lgkmcnt(0)" ::: "memory"); AT_SBAR();
;     ...
;     od = __builtin_amdgcn_mfma_f32_32x32x16_bf16(AT_PK(l0, h0), pa0, od, 0, 0, 0);
;     od = __builtin_amdgcn_mfma_f32_32x32x16_bf16(AT_PK(l1, h1), pa1, od, 0, 0, 0);
;     od = __builtin_amdgcn_mfma_f32_32x32x16_bf16(AT_PK(l2, h2), pa2, od, 0, 0, 0);
;     od = __builtin_amdgcn_mfma_f32_32x32x16_bf16(AT_PK(l3, h3), pa3, od, 0, 0, 0);
;     ...
; }
; DI void pv_all_sm(f32x16* o, int vb, bf16x8 pa0, bf16x8 pa1, bf16x8 pa2, bf16x8 pa3, f32x16& p0, f32x16& p1, float& m_ref, f32x16& negm, float& alpha) {
;     pv_one<0>(o[0], vb, pa0, pa1, pa2, pa3);
;     float pmax = p0[0];
; #pragma unroll
;     for (int r = 1; r < 16; ++r) pmax = fmaxf(pmax, p0[r]);
;     pv_one<1>(o[1], vb, pa0, pa1, pa2, pa3);
; #pragma unroll
;     for (int r = 0; r < 16; ++r) pmax = fmaxf(pmax, p1[r]);
;     { auto rr = __builtin_amdgcn_permlane32_swap(__float_as_uint(pmax), __float_as_uint(pmax), false, false); pmax = fmaxf(__uint_as_float(rr[0]), __uint_as_float(rr[1])); }
;     pv_one<2>(o[2], vb, pa0, pa1, pa2, pa3);
;     alpha = 1.f;
;     if (__builtin_expect(!__all(pmax <= THRL), 0)) {
.LBB4_872:
	ds_read_b64_tr_b16 v[224:225], v215 offset:0x2000
	ds_read_b64_tr_b16 v[226:227], v215 offset:0x2100
	ds_read_b64_tr_b16 v[228:229], v215 offset:0x3000
	ds_read_b64_tr_b16 v[230:231], v215 offset:0x3100
	s_waitcnt lgkmcnt(0)
	v_mfma_f32_32x32x16_bf16 v[32:47], v[216:219], v[120:123], v[32:47]
	v_max_f32_e32 v182, v128, v129
	ds_read_b64_tr_b16 v[216:217], v215 offset:0x200
	ds_read_b64_tr_b16 v[218:219], v215 offset:0x300
	v_max3_f32 v182, v182, v130, v131
	v_max3_f32 v182, v182, v132, v133
	v_mfma_f32_32x32x16_bf16 v[32:47], v[220:223], v[124:127], v[32:47]
	ds_read_b64_tr_b16 v[220:221], v215 offset:0x1200
	ds_read_b64_tr_b16 v[222:223], v215 offset:0x1300
	v_max3_f32 v182, v182, v134, v135
	v_max3_f32 v182, v182, v136, v137
	v_max3_f32 v182, v182, v138, v139
	v_max3_f32 v182, v182, v140, v141
	v_max3_f32 v182, v182, v142, v143
	v_mfma_f32_32x32x16_bf16 v[32:47], v[224:227], v[112:115], v[32:47]
	ds_read_b64_tr_b16 v[224:225], v215 offset:0x2200
	ds_read_b64_tr_b16 v[226:227], v215 offset:0x2300
	ds_read_b64_tr_b16 v[232:233], v215 offset:0x3200
	ds_read_b64_tr_b16 v[234:235], v215 offset:0x3300
	v_mfma_f32_32x32x16_bf16 v[32:47], v[228:231], v[116:119], v[32:47]
	s_waitcnt lgkmcnt(0)
	v_mfma_f32_32x32x16_bf16 v[48:63], v[216:219], v[120:123], v[48:63]
	v_max3_f32 v182, v182, v96, v97
	v_max3_f32 v182, v182, v98, v99
	ds_read_b64_tr_b16 v[218:219], v215 offset:0x400
	v_max3_f32 v182, v182, v100, v101
	v_max3_f32 v182, v182, v102, v103
	v_max3_f32 v182, v182, v104, v105
	v_max3_f32 v182, v182, v106, v107
	v_mfma_f32_32x32x16_bf16 v[48:63], v[220:223], v[124:127], v[48:63]
	ds_read_b64_tr_b16 v[220:221], v215 offset:0x500
	ds_read_b64_tr_b16 v[222:223], v215 offset:0x1400
	v_max3_f32 v182, v182, v108, v109
	v_max3_f32 v182, v182, v110, v111
	v_mov_b32_e32 v216, v182
	s_nop 1
	v_permlane32_swap_b32_e32 v182, v216
	v_mfma_f32_32x32x16_bf16 v[48:63], v[224:227], v[112:115], v[48:63]
	ds_read_b64_tr_b16 v[224:225], v215 offset:0x1500
	ds_read_b64_tr_b16 v[226:227], v215 offset:0x2400
	ds_read_b64_tr_b16 v[228:229], v215 offset:0x2500
	ds_read_b64_tr_b16 v[236:237], v215 offset:0x3400
	ds_read_b64_tr_b16 v[238:239], v215 offset:0x3500
	v_mfma_f32_32x32x16_bf16 v[48:63], v[232:235], v[116:119], v[48:63]
	s_waitcnt lgkmcnt(0)
	v_max_f32_e32 v216, v182, v216
	v_mfma_f32_32x32x16_bf16 v[16:31], v[218:221], v[120:123], v[16:31]
	v_cmp_ge_f32_e32 vcc, s15, v216
	s_cmp_eq_u64 vcc, exec
	v_mov_b32_e32 v182, 1.0
	v_mfma_f32_32x32x16_bf16 v[16:31], v[222:225], v[124:127], v[16:31]
	v_mfma_f32_32x32x16_bf16 v[16:31], v[226:229], v[112:115], v[16:31]
	v_mfma_f32_32x32x16_bf16 v[16:31], v[236:239], v[116:119], v[16:31]
	s_cbranch_scc0 .LBB4_885

; template <int OFF> DI s16x4 tr_read(int vb) { s16x4 r; asm volatile("ds_read_b64_tr_b16 %0, %1 offset:%2" : "=&v"(r) : "v"(vb), "i"(OFF) : "memory"); return r; }
; DI void finishSM(f32x16& p0, f32x16& p1, float alpha, float& l_reg, bf16x8& pa0, bf16x8& pa1, bf16x8& pa2, bf16x8& pa3) {
; #pragma unroll
;     for (int r = 0; r < 16; ++r) p1[r] = __builtin_amdgcn_exp2f(p1[r]);
;     float ps = 0;
; #pragma unroll
;     for (int r = 0; r < 16; ++r) ps += p0[r];
; #pragma unroll
;     for (int r = 0; r < 16; ++r) ps += p1[r];
;     { auto rr = __builtin_amdgcn_permlane32_swap(__float_as_uint(ps), __float_as_uint(ps), false, false); ps = __uint_as_float(rr[0]) + __uint_as_float(rr[1]); }
;     l_reg = l_reg * alpha + ps;
;     ...
;     AT_PK4(p0, 0, pa0); AT_PK4(p0, 8, pa1); AT_PK4(p1, 0, pa2); AT_PK4(p1, 8, pa3);
;     ...
; }
; DI void qkt(f32x16& p0, f32x16& p1, const char* Ks, const bf16x8* qr, const f32x16& negm, int r32, int hi) {
; #pragma unroll
;     for (int d0 = 0; d0 < 4; ++d0) { const int cb = (d0 * 16 + hi * 8) * 2;
;         const bf16x8 b0 = *reinterpret_cast<const bf16x8*>(Ks + AT_KSWZ(r32, cb));
;         const bf16x8 b1 = *reinterpret_cast<const bf16x8*>(Ks + AT_KSWZ(32 + r32, cb));
;         p0 = __builtin_amdgcn_mfma_f32_32x32x16_bf16(b0, qr[d0], d0 == 0 ? negm : p0, 0, 0, 0);
;         p1 = __builtin_amdgcn_mfma_f32_32x32x16_bf16(b1, qr[d0], d0 == 0 ? negm : p1, 0, 0, 0); }
; }
; template <int D0> DI void pv_one(f32x16& od, int vb, bf16x8 pa0, bf16x8 pa1, bf16x8 pa2, bf16x8 pa3) {
;     const s16x4 l0 = tr_read<v_rd_off(D0, 0, 0)>(vb), h0 = tr_read<v_rd_off(D0, 0, 1)>(vb), l1 = tr_read<v_rd_off(D0, 1, 0)>(vb), h1 = tr_read<v_rd_off(D0, 1, 1)>(vb);
;     const s16x4 l2 = tr_read<v_rd_off(D0, 2, 0)>(vb), h2 = tr_read<v_rd_off(D0, 2, 1)>(vb), l3 = tr_read<v_rd_off(D0, 3, 0)>(vb), h3 = tr_read<v_rd_off(D0, 3, 1)>(vb);
.LBB4_923:
	s_lshl_b32 s18, s30, 13
	s_add_i32 s18, s18, 0
	v_add_u32_e32 v72, s18, v208
	v_add_u32_e32 v112, s18, v209
	v_add_u32_e32 v180, s18, v210
	s_waitcnt lgkmcnt(1)
	v_mfma_f32_32x32x16_bf16 v[128:143], v[64:67], v[156:159], v[80:95]
	ds_read_b128 v[64:67], v72 offset:49152
	ds_read_b128 v[72:75], v72 offset:53248
	ds_read_b128 v[76:79], v112 offset:49152
	ds_read_b128 v[224:227], v112 offset:53248
	s_add_u32 s34, s46, s16
	s_addc_u32 s35, s47, s17
	s_add_u32 s24, s34, 0x23808000
	s_addc_u32 s25, s35, 0
	s_add_u32 s54, s34, 0x2380a000
	s_add_u32 s42, s46, s20
	s_addc_u32 s43, s47, s21
	s_add_u32 s56, s42, 0x21884000
	s_addc_u32 s57, s43, 0
	s_lshl_b32 s92, s15, 14
	s_add_i32 s92, s92, s94
	s_mov_b32 m0, s92
	s_lshl_b32 s96, s15, 13
	global_load_lds_dwordx4 v249, s[24:25]
	s_addk_i32 s92, 0x400
	s_mov_b32 m0, s92
	s_add_i32 s96, s96, s95
	global_load_lds_dwordx4 v250, s[24:25]
	s_nop 0
	s_mov_b32 m0, s96
	s_nop 0
	global_load_lds_dwordx4 v251, s[56:57]
	v_exp_f32_e32 v182, v97
	v_exp_f32_e32 v217, v98
	v_exp_f32_e32 v218, v99
	v_exp_f32_e32 v223, v100
	v_exp_f32_e32 v232, v101
	s_waitcnt lgkmcnt(4)
	v_mfma_f32_32x32x16_bf16 v[112:127], v[68:71], v[156:159], v[80:95]
	ds_read_b128 v[68:71], v180 offset:49152
	ds_read_b128 v[228:231], v180 offset:53248
	v_exp_f32_e32 v180, v96
	v_cvt_pk_bf16_f32 v96, v220, v222
	v_cvt_pk_bf16_f32 v97, v179, v221
	v_cvt_pk_bf16_f32 v98, v177, v219
	v_cvt_pk_bf16_f32 v99, v176, v178
	s_waitcnt lgkmcnt(4)
	v_mfma_f32_32x32x16_bf16 v[112:127], v[72:75], v[152:155], v[112:127]
	v_add_f32_e32 v75, 0, v220
	v_add_f32_e32 v75, v222, v75
	v_add_f32_e32 v75, v179, v75
	v_add_f32_e32 v75, v221, v75
	v_add_f32_e32 v75, v177, v75
	v_add_f32_e32 v75, v219, v75
	v_add_f32_e32 v75, v176, v75
	v_mfma_f32_32x32x16_bf16 v[128:143], v[64:67], v[152:155], v[128:143]
	v_add_f32_e32 v75, v178, v75
	v_add_f32_e32 v75, v173, v75
	v_add_f32_e32 v75, v175, v75
	v_add_f32_e32 v75, v171, v75
	v_add_f32_e32 v75, v174, v75
	v_add_f32_e32 v75, v169, v75
	v_add_f32_e32 v75, v172, v75
	s_waitcnt lgkmcnt(3)
	v_mfma_f32_32x32x16_bf16 v[128:143], v[76:79], v[148:151], v[128:143]
	v_add_f32_e32 v75, v168, v75
	v_add_f32_e32 v75, v170, v75
	v_add_f32_e32 v75, v180, v75
	v_add_f32_e32 v75, v182, v75
	v_exp_f32_e32 v64, v102
	v_exp_f32_e32 v65, v103
	v_exp_f32_e32 v66, v104
	s_waitcnt lgkmcnt(2)
	v_mfma_f32_32x32x16_bf16 v[112:127], v[224:227], v[148:151], v[112:127]
	v_exp_f32_e32 v67, v105
	v_exp_f32_e32 v105, v106
	v_exp_f32_e32 v106, v107
	v_exp_f32_e32 v107, v108
	v_exp_f32_e32 v72, v109
	v_exp_f32_e32 v73, v110
	v_exp_f32_e32 v74, v111
	s_waitcnt lgkmcnt(1)
	v_mfma_f32_32x32x16_bf16 v[128:143], v[68:71], v[144:147], v[128:143]
	v_add_f32_e32 v68, v217, v75
	v_add_f32_e32 v68, v218, v68
	v_add_f32_e32 v68, v223, v68
	v_add_f32_e32 v68, v232, v68
	v_add_f32_e32 v68, v64, v68
	v_add_f32_e32 v68, v65, v68
	v_add_f32_e32 v68, v66, v68
	v_add_f32_e32 v68, v67, v68
	s_waitcnt lgkmcnt(0)
	v_mfma_f32_32x32x16_bf16 v[112:127], v[228:231], v[144:147], v[112:127]
	v_cvt_pk_bf16_f32 v100, v180, v182
	v_cvt_pk_bf16_f32 v103, v64, v65
	v_cvt_pk_bf16_f32 v104, v66, v67
	s_lshl_b32 s31, s29, 14
	v_add_u32_e32 v182, s31, v253
	ds_read_b64_tr_b16 v[64:65], v182 offset:0
	ds_read_b64_tr_b16 v[66:67], v182 offset:0x100
	v_add_f32_e32 v68, v105, v68
	v_add_f32_e32 v68, v106, v68
	v_add_f32_e32 v68, v107, v68
	v_add_f32_e32 v68, v72, v68
	v_add_f32_e32 v68, v73, v68
	v_add_f32_e32 v215, v74, v68
	ds_read_b64_tr_b16 v[68:69], v182 offset:0x1000
	ds_read_b64_tr_b16 v[70:71], v182 offset:0x1100
	v_cvt_pk_bf16_f32 v108, v173, v175
	v_cvt_pk_bf16_f32 v109, v171, v174
	v_cvt_pk_bf16_f32 v110, v169, v172
	v_cvt_pk_bf16_f32 v111, v168, v170
	v_cvt_pk_bf16_f32 v101, v217, v218
	v_cvt_pk_bf16_f32 v102, v223, v232
	v_cvt_pk_bf16_f32 v105, v105, v106
	v_cvt_pk_bf16_f32 v106, v107, v72
	v_cvt_pk_bf16_f32 v107, v73, v74
	s_addc_u32 s55, s35, 0
	s_andn2_b64 vcc, exec, s[2:3]
	s_cbranch_vccnz .LBB4_925
	s_mov_b64 s[2:3], s[8:9]
	global_store_dwordx2 v193, v[184:185], s[2:3] nt

; template <int OFF> DI s16x4 tr_read(int vb) { s16x4 r; asm volatile("ds_read_b64_tr_b16 %0, %1 offset:%2" : "=&v"(r) : "v"(vb), "i"(OFF) : "memory"); return r; }
; DI void finishSM(f32x16& p0, f32x16& p1, float alpha, float& l_reg, bf16x8& pa0, bf16x8& pa1, bf16x8& pa2, bf16x8& pa3) {
; #pragma unroll
;     for (int r = 0; r < 16; ++r) p1[r] = __builtin_amdgcn_exp2f(p1[r]);
;     float ps = 0;
; #pragma unroll
;     for (int r = 0; r < 16; ++r) ps += p0[r];
; #pragma unroll
;     for (int r = 0; r < 16; ++r) ps += p1[r];
;     { auto rr = __builtin_amdgcn_permlane32_swap(__float_as_uint(ps), __float_as_uint(ps), false, false); ps = __uint_as_float(rr[0]) + __uint_as_float(rr[1]); }
;     l_reg = l_reg * alpha + ps;
;     ...
;     AT_PK4(p0, 0, pa0); AT_PK4(p0, 8, pa1); AT_PK4(p1, 0, pa2); AT_PK4(p1, 8, pa3);
;     ...
; }
; DI void qkt(f32x16& p0, f32x16& p1, const char* Ks, const bf16x8* qr, const f32x16& negm, int r32, int hi) {
; #pragma unroll
;     for (int d0 = 0; d0 < 4; ++d0) { const int cb = (d0 * 16 + hi * 8) * 2;
;         const bf16x8 b0 = *reinterpret_cast<const bf16x8*>(Ks + AT_KSWZ(r32, cb));
;         const bf16x8 b1 = *reinterpret_cast<const bf16x8*>(Ks + AT_KSWZ(32 + r32, cb));
;         p0 = __builtin_amdgcn_mfma_f32_32x32x16_bf16(b0, qr[d0], d0 == 0 ? negm : p0, 0, 0, 0);
;         p1 = __builtin_amdgcn_mfma_f32_32x32x16_bf16(b1, qr[d0], d0 == 0 ? negm : p1, 0, 0, 0); }
; }
; template <int D0> DI void pv_one(f32x16& od, int vb, bf16x8 pa0, bf16x8 pa1, bf16x8 pa2, bf16x8 pa3) {
;     const s16x4 l0 = tr_read<v_rd_off(D0, 0, 0)>(vb), h0 = tr_read<v_rd_off(D0, 0, 1)>(vb), l1 = tr_read<v_rd_off(D0, 1, 0)>(vb), h1 = tr_read<v_rd_off(D0, 1, 1)>(vb);
;     const s16x4 l2 = tr_read<v_rd_off(D0, 2, 0)>(vb), h2 = tr_read<v_rd_off(D0, 2, 1)>(vb), l3 = tr_read<v_rd_off(D0, 3, 0)>(vb), h3 = tr_read<v_rd_off(D0, 3, 1)>(vb);
.LBB4_944:
	v_exp_f32_e32 v182, v128
	v_exp_f32_e32 v234, v129
	v_exp_f32_e32 v235, v130
	v_exp_f32_e32 v236, v131
	v_exp_f32_e32 v237, v132
	v_exp_f32_e32 v238, v133
	v_exp_f32_e32 v239, v134
	v_exp_f32_e32 v240, v135
	v_exp_f32_e32 v241, v136
	v_exp_f32_e32 v242, v137
	v_exp_f32_e32 v243, v138
	v_exp_f32_e32 v244, v139
	v_exp_f32_e32 v245, v140
	v_exp_f32_e32 v246, v141
	v_exp_f32_e32 v247, v142
	v_exp_f32_e32 v248, v143
	v_add_u32_e32 v101, s54, v208
	v_add_u32_e32 v102, s54, v209
	v_add_u32_e32 v103, s54, v210
	ds_read_b128 v[172:175], v101 offset:49152
	ds_read_b128 v[176:179], v101 offset:53248
	ds_read_b128 v[218:221], v102 offset:49152
	ds_read_b128 v[222:225], v102 offset:53248
	ds_read_b128 v[226:229], v103 offset:49152
	ds_read_b128 v[230:233], v103 offset:53248
	v_exp_f32_e32 v112, v112
	v_exp_f32_e32 v113, v113
	v_exp_f32_e32 v114, v114
	s_waitcnt lgkmcnt(7)
	v_mfma_f32_32x32x16_bf16 v[128:143], v[96:99], v[156:159], v[80:95]
	s_add_u32 s24, s34, 0x2380c000
	s_addc_u32 s25, s35, 0
	s_add_u32 s34, s34, 0x2380e000
	s_addc_u32 s35, s35, 0
	s_add_u32 s42, s42, 0x21886000
	s_addc_u32 s43, s43, 0
	s_lshl_b32 s92, s29, 14
	s_add_i32 s92, s92, s94
	s_mov_b32 m0, s92
	s_lshl_b32 s96, s29, 13
	global_load_lds_dwordx4 v249, s[24:25]
	s_addk_i32 s92, 0x400
	s_mov_b32 m0, s92
	s_add_i32 s96, s96, s95
	global_load_lds_dwordx4 v250, s[24:25]
	s_nop 0
	s_mov_b32 m0, s96
	s_nop 0
	global_load_lds_dwordx4 v251, s[42:43]
	s_nop 0
	v_exp_f32_e32 v115, v115
	v_exp_f32_e32 v116, v116
	v_exp_f32_e32 v117, v117
	v_exp_f32_e32 v118, v118
	v_exp_f32_e32 v119, v119
	s_waitcnt lgkmcnt(6)
	v_mfma_f32_32x32x16_bf16 v[96:111], v[168:171], v[156:159], v[80:95]
	v_exp_f32_e32 v168, v120
	v_add_f32_e32 v120, 0, v182
	v_add_f32_e32 v120, v234, v120
	v_add_f32_e32 v120, v235, v120
	v_add_f32_e32 v120, v236, v120
	v_add_f32_e32 v120, v237, v120
	v_add_f32_e32 v120, v238, v120
	v_add_f32_e32 v120, v239, v120
	v_add_f32_e32 v120, v240, v120
	v_add_f32_e32 v120, v241, v120
	v_add_f32_e32 v120, v242, v120
	s_waitcnt lgkmcnt(5)
	v_mfma_f32_32x32x16_bf16 v[128:143], v[172:175], v[152:155], v[128:143]
	v_add_f32_e32 v120, v243, v120
	v_add_f32_e32 v120, v244, v120
	v_add_f32_e32 v120, v245, v120
	v_add_f32_e32 v120, v246, v120
	v_add_f32_e32 v120, v247, v120
	v_add_f32_e32 v120, v248, v120
	v_add_f32_e32 v120, v112, v120
	s_waitcnt lgkmcnt(4)
	v_mfma_f32_32x32x16_bf16 v[96:111], v[176:179], v[152:155], v[96:111]
	v_add_f32_e32 v120, v113, v120
	v_add_f32_e32 v120, v114, v120
	v_add_f32_e32 v120, v115, v120
	v_add_f32_e32 v120, v116, v120
	v_exp_f32_e32 v169, v121
	v_add_f32_e32 v120, v117, v120
	v_exp_f32_e32 v170, v122
	s_waitcnt lgkmcnt(3)
	v_mfma_f32_32x32x16_bf16 v[128:143], v[218:221], v[148:151], v[128:143]
	v_add_f32_e32 v120, v118, v120
	v_exp_f32_e32 v171, v123
	v_add_f32_e32 v120, v119, v120
	v_exp_f32_e32 v172, v124
	v_add_f32_e32 v120, v168, v120
	v_exp_f32_e32 v173, v125
	v_add_f32_e32 v120, v169, v120
	s_waitcnt lgkmcnt(2)
	v_mfma_f32_32x32x16_bf16 v[96:111], v[222:225], v[148:151], v[96:111]
	v_exp_f32_e32 v174, v126
	v_add_f32_e32 v120, v170, v120
	v_exp_f32_e32 v175, v127
	v_add_f32_e32 v120, v171, v120
	v_add_f32_e32 v120, v172, v120
	v_add_f32_e32 v120, v173, v120
	v_add_f32_e32 v120, v174, v120
	s_waitcnt lgkmcnt(1)
	v_mfma_f32_32x32x16_bf16 v[128:143], v[226:229], v[144:147], v[128:143]
	v_add_f32_e32 v217, v175, v120
	v_cvt_pk_bf16_f32 v120, v182, v234
	v_cvt_pk_bf16_f32 v121, v235, v236
	v_cvt_pk_bf16_f32 v122, v237, v238
	v_cvt_pk_bf16_f32 v123, v239, v240
	v_cvt_pk_bf16_f32 v124, v241, v242
	s_waitcnt lgkmcnt(0)
	v_mfma_f32_32x32x16_bf16 v[96:111], v[230:233], v[144:147], v[96:111]
	v_lshl_add_u32 v219, s30, 14, v253
	ds_read_b64_tr_b16 v[220:221], v219 offset:0
	ds_read_b64_tr_b16 v[222:223], v219 offset:0x100
	ds_read_b64_tr_b16 v[224:225], v219 offset:0x1000
	ds_read_b64_tr_b16 v[226:227], v219 offset:0x1100
	v_cvt_pk_bf16_f32 v125, v243, v244
	v_cvt_pk_bf16_f32 v126, v245, v246
	v_cvt_pk_bf16_f32 v127, v247, v248
	v_cvt_pk_bf16_f32 v112, v112, v113
	v_cvt_pk_bf16_f32 v113, v114, v115
	v_cvt_pk_bf16_f32 v114, v116, v117
	v_cvt_pk_bf16_f32 v115, v118, v119
	v_cvt_pk_bf16_f32 v116, v168, v169
	v_cvt_pk_bf16_f32 v117, v170, v171
	v_cvt_pk_bf16_f32 v118, v172, v173
	v_cvt_pk_bf16_f32 v119, v174, v175
	s_and_b64 vcc, exec, s[2:3]
	s_cbranch_vccnz .LBB4_946
	s_mov_b64 s[2:3], s[8:9]
	global_store_dwordx2 v193, v[184:185], s[2:3] nt
